# best3 with chains ordered so four consecutive chains share the A-fragment pair
# speedup vs baseline: 1.0196x; 1.0015x over previous
.LBB0_130:
	ds_read_b128 v[144:147], v140
	ds_read_b128 v[148:151], v140 offset:1024
	ds_read_b128 v[152:155], v140 offset:2048
	ds_read_b128 v[156:159], v140 offset:3072
	ds_read_b128 v[164:167], v141
	ds_read_b128 v[168:171], v141 offset:1024
	ds_read_b128 v[172:175], v141 offset:2048
	ds_read_b128 v[176:179], v141 offset:3072
	s_add_u32 s31, s10, 0xfff7c080
	s_addc_u32 s53, s11, -1
	s_cmp_eq_u32 s30, 28
	s_cselect_b32 s55, s25, s53
	s_cselect_b32 s54, s24, s31
	s_cselect_b32 s57, s4, s29
	s_cselect_b32 s56, s5, s28
	s_mov_b32 m0, s23
	v_lshl_add_u64 v[184:185], s[10:11], 0, v[138:139]
	ds_read_b128 v[180:183], v163
	ds_read_b128 v[190:193], v163 offset:1024
	ds_read_b128 v[194:197], v163 offset:2048
	ds_read_b128 v[198:201], v163 offset:3072
	ds_read_b128 v[202:205], v163 offset:4096
	ds_read_b128 v[206:209], v163 offset:5120
	ds_read_b128 v[216:219], v163 offset:6144
	ds_read_b128 v[220:223], v163 offset:7168
	global_load_lds_dwordx4 v[184:185], off
	v_lshl_add_u64 v[184:185], v[184:185], 0, s[96:97]
	s_mov_b32 m0, s33
	s_nop 0
	global_load_lds_dwordx4 v[184:185], off
	s_waitcnt vmcnt(8)
	s_waitcnt lgkmcnt(0)
	s_barrier
	v_mfma_f32_16x16x32_bf16 v[120:123], v[144:147], v[180:183], v[120:123]
	v_mfma_f32_16x16x32_bf16 v[120:123], v[148:151], v[190:193], v[120:123]
	v_mfma_f32_16x16x32_bf16 v[116:119], v[152:155], v[180:183], v[116:119]
	v_mfma_f32_16x16x32_bf16 v[116:119], v[156:159], v[190:193], v[116:119]
	v_mfma_f32_16x16x32_bf16 v[128:131], v[164:167], v[180:183], v[128:131]
	v_mfma_f32_16x16x32_bf16 v[128:131], v[168:171], v[190:193], v[128:131]
	v_mfma_f32_16x16x32_bf16 v[124:127], v[172:175], v[180:183], v[124:127]
	v_mfma_f32_16x16x32_bf16 v[124:127], v[176:179], v[190:193], v[124:127]
	v_mfma_f32_16x16x32_bf16 v[104:107], v[144:147], v[194:197], v[104:107]
	v_mfma_f32_16x16x32_bf16 v[104:107], v[148:151], v[198:201], v[104:107]
	v_mfma_f32_16x16x32_bf16 v[100:103], v[152:155], v[194:197], v[100:103]
	v_mfma_f32_16x16x32_bf16 v[100:103], v[156:159], v[198:201], v[100:103]
	v_mfma_f32_16x16x32_bf16 v[112:115], v[164:167], v[194:197], v[112:115]
	v_mfma_f32_16x16x32_bf16 v[112:115], v[168:171], v[198:201], v[112:115]
	v_mfma_f32_16x16x32_bf16 v[108:111], v[172:175], v[194:197], v[108:111]
	v_mfma_f32_16x16x32_bf16 v[108:111], v[176:179], v[198:201], v[108:111]
	v_mfma_f32_16x16x32_bf16 v[88:91], v[144:147], v[202:205], v[88:91]
	v_mfma_f32_16x16x32_bf16 v[88:91], v[148:151], v[206:209], v[88:91]
	v_mfma_f32_16x16x32_bf16 v[84:87], v[152:155], v[202:205], v[84:87]
	v_mfma_f32_16x16x32_bf16 v[84:87], v[156:159], v[206:209], v[84:87]
	v_mfma_f32_16x16x32_bf16 v[96:99], v[164:167], v[202:205], v[96:99]
	v_mfma_f32_16x16x32_bf16 v[96:99], v[168:171], v[206:209], v[96:99]
	v_mfma_f32_16x16x32_bf16 v[92:95], v[172:175], v[202:205], v[92:95]
	v_mfma_f32_16x16x32_bf16 v[92:95], v[176:179], v[206:209], v[92:95]
	v_mfma_f32_16x16x32_bf16 v[72:75], v[144:147], v[216:219], v[72:75]
	v_mfma_f32_16x16x32_bf16 v[72:75], v[148:151], v[220:223], v[72:75]
	v_mfma_f32_16x16x32_bf16 v[68:71], v[152:155], v[216:219], v[68:71]
	v_mfma_f32_16x16x32_bf16 v[68:71], v[156:159], v[220:223], v[68:71]
	v_mfma_f32_16x16x32_bf16 v[80:83], v[164:167], v[216:219], v[80:83]
	v_mfma_f32_16x16x32_bf16 v[80:83], v[168:171], v[220:223], v[80:83]
	v_mfma_f32_16x16x32_bf16 v[76:79], v[172:175], v[216:219], v[76:79]
	v_mfma_f32_16x16x32_bf16 v[76:79], v[176:179], v[220:223], v[76:79]
	s_barrier
	s_mov_b32 m0, s45
	v_lshl_add_u64 v[184:185], s[56:57], 0, v[132:133]
	ds_read_b128 v[180:183], v163 offset:16384
	ds_read_b128 v[190:193], v163 offset:17408
	ds_read_b128 v[194:197], v163 offset:18432
	ds_read_b128 v[198:201], v163 offset:19456
	ds_read_b128 v[202:205], v163 offset:20480
	ds_read_b128 v[206:209], v163 offset:21504
	ds_read_b128 v[216:219], v163 offset:22528
	ds_read_b128 v[220:223], v163 offset:23552
	global_load_lds_dwordx4 v[184:185], off
	v_lshl_add_u64 v[186:187], v[184:185], 0, s[90:91]
	s_mov_b32 m0, s46
	s_nop 0
	global_load_lds_dwordx4 v[186:187], off
	v_lshl_add_u64 v[186:187], v[184:185], 0, s[60:61]
	s_mov_b32 m0, s47
	s_nop 0
	global_load_lds_dwordx4 v[186:187], off
	v_lshl_add_u64 v[186:187], v[184:185], 0, s[64:65]
	s_mov_b32 m0, s48
	s_nop 0
	global_load_lds_dwordx4 v[186:187], off
	v_lshl_add_u64 v[186:187], s[54:55], 0, v[134:135]
	s_mov_b32 m0, s37
	v_lshl_add_u64 v[188:189], v[186:187], 0, s[96:97]
	global_load_lds_dwordx4 v[186:187], off
	s_mov_b32 m0, s38
	s_nop 0
	global_load_lds_dwordx4 v[188:189], off
	s_waitcnt vmcnt(8)
	s_waitcnt lgkmcnt(0)
	s_barrier
	v_mfma_f32_16x16x32_bf16 v[56:59], v[144:147], v[180:183], v[56:59]
	v_mfma_f32_16x16x32_bf16 v[56:59], v[148:151], v[190:193], v[56:59]
	v_mfma_f32_16x16x32_bf16 v[52:55], v[152:155], v[180:183], v[52:55]
	v_mfma_f32_16x16x32_bf16 v[52:55], v[156:159], v[190:193], v[52:55]
	v_mfma_f32_16x16x32_bf16 v[64:67], v[164:167], v[180:183], v[64:67]
	v_mfma_f32_16x16x32_bf16 v[64:67], v[168:171], v[190:193], v[64:67]
	v_mfma_f32_16x16x32_bf16 v[60:63], v[172:175], v[180:183], v[60:63]
	v_mfma_f32_16x16x32_bf16 v[60:63], v[176:179], v[190:193], v[60:63]
	v_mfma_f32_16x16x32_bf16 v[40:43], v[144:147], v[194:197], v[40:43]
	v_mfma_f32_16x16x32_bf16 v[40:43], v[148:151], v[198:201], v[40:43]
	v_mfma_f32_16x16x32_bf16 v[36:39], v[152:155], v[194:197], v[36:39]
	v_mfma_f32_16x16x32_bf16 v[36:39], v[156:159], v[198:201], v[36:39]
	v_mfma_f32_16x16x32_bf16 v[48:51], v[164:167], v[194:197], v[48:51]
	v_mfma_f32_16x16x32_bf16 v[48:51], v[168:171], v[198:201], v[48:51]
	v_mfma_f32_16x16x32_bf16 v[44:47], v[172:175], v[194:197], v[44:47]
	v_mfma_f32_16x16x32_bf16 v[44:47], v[176:179], v[198:201], v[44:47]
	v_mfma_f32_16x16x32_bf16 v[24:27], v[144:147], v[202:205], v[24:27]
	v_mfma_f32_16x16x32_bf16 v[24:27], v[148:151], v[206:209], v[24:27]
	v_mfma_f32_16x16x32_bf16 v[20:23], v[152:155], v[202:205], v[20:23]
	v_mfma_f32_16x16x32_bf16 v[20:23], v[156:159], v[206:209], v[20:23]
	v_mfma_f32_16x16x32_bf16 v[32:35], v[164:167], v[202:205], v[32:35]
	v_mfma_f32_16x16x32_bf16 v[32:35], v[168:171], v[206:209], v[32:35]
	v_mfma_f32_16x16x32_bf16 v[28:31], v[172:175], v[202:205], v[28:31]
	v_mfma_f32_16x16x32_bf16 v[28:31], v[176:179], v[206:209], v[28:31]
	v_mfma_f32_16x16x32_bf16 v[8:11], v[144:147], v[216:219], v[8:11]
	v_mfma_f32_16x16x32_bf16 v[8:11], v[148:151], v[220:223], v[8:11]
	v_mfma_f32_16x16x32_bf16 v[4:7], v[152:155], v[216:219], v[4:7]
	v_mfma_f32_16x16x32_bf16 v[4:7], v[156:159], v[220:223], v[4:7]
	v_mfma_f32_16x16x32_bf16 v[16:19], v[164:167], v[216:219], v[16:19]
	v_mfma_f32_16x16x32_bf16 v[16:19], v[168:171], v[220:223], v[16:19]
	v_mfma_f32_16x16x32_bf16 v[12:15], v[172:175], v[216:219], v[12:15]
	v_mfma_f32_16x16x32_bf16 v[12:15], v[176:179], v[220:223], v[12:15]
	s_barrier
	ds_read_b128 v[144:147], v142
	ds_read_b128 v[148:151], v142 offset:1024
	ds_read_b128 v[152:155], v142 offset:2048
	ds_read_b128 v[156:159], v142 offset:3072
	ds_read_b128 v[164:167], v143
	ds_read_b128 v[168:171], v143 offset:1024
	ds_read_b128 v[172:175], v143 offset:2048
	ds_read_b128 v[176:179], v143 offset:3072
	s_mov_b32 m0, s39
	v_lshl_add_u64 v[188:189], v[186:187], 0, s[82:83]
	ds_read_b128 v[180:183], v163 offset:32768
	ds_read_b128 v[190:193], v163 offset:33792
	ds_read_b128 v[194:197], v163 offset:34816
	ds_read_b128 v[198:201], v163 offset:35840
	ds_read_b128 v[202:205], v163 offset:36864
	ds_read_b128 v[206:209], v163 offset:37888
	ds_read_b128 v[216:219], v163 offset:38912
	ds_read_b128 v[220:223], v163 offset:39936
	global_load_lds_dwordx4 v[188:189], off
	v_lshl_add_u64 v[188:189], v[186:187], 0, s[68:69]
	s_mov_b32 m0, s40
	s_nop 0
	global_load_lds_dwordx4 v[188:189], off
	s_waitcnt vmcnt(8)
	s_waitcnt lgkmcnt(0)
	s_barrier
	v_mfma_f32_16x16x32_bf16 v[120:123], v[144:147], v[180:183], v[120:123]
	v_mfma_f32_16x16x32_bf16 v[120:123], v[148:151], v[190:193], v[120:123]
	v_mfma_f32_16x16x32_bf16 v[116:119], v[152:155], v[180:183], v[116:119]
	v_mfma_f32_16x16x32_bf16 v[116:119], v[156:159], v[190:193], v[116:119]
	v_mfma_f32_16x16x32_bf16 v[128:131], v[164:167], v[180:183], v[128:131]
	v_mfma_f32_16x16x32_bf16 v[128:131], v[168:171], v[190:193], v[128:131]
	v_mfma_f32_16x16x32_bf16 v[124:127], v[172:175], v[180:183], v[124:127]
	v_mfma_f32_16x16x32_bf16 v[124:127], v[176:179], v[190:193], v[124:127]
	v_mfma_f32_16x16x32_bf16 v[104:107], v[144:147], v[194:197], v[104:107]
	v_mfma_f32_16x16x32_bf16 v[104:107], v[148:151], v[198:201], v[104:107]
	v_mfma_f32_16x16x32_bf16 v[100:103], v[152:155], v[194:197], v[100:103]
	v_mfma_f32_16x16x32_bf16 v[100:103], v[156:159], v[198:201], v[100:103]
	v_mfma_f32_16x16x32_bf16 v[112:115], v[164:167], v[194:197], v[112:115]
	v_mfma_f32_16x16x32_bf16 v[112:115], v[168:171], v[198:201], v[112:115]
	v_mfma_f32_16x16x32_bf16 v[108:111], v[172:175], v[194:197], v[108:111]
	v_mfma_f32_16x16x32_bf16 v[108:111], v[176:179], v[198:201], v[108:111]
	v_mfma_f32_16x16x32_bf16 v[88:91], v[144:147], v[202:205], v[88:91]
	v_mfma_f32_16x16x32_bf16 v[88:91], v[148:151], v[206:209], v[88:91]
	v_mfma_f32_16x16x32_bf16 v[84:87], v[152:155], v[202:205], v[84:87]
	v_mfma_f32_16x16x32_bf16 v[84:87], v[156:159], v[206:209], v[84:87]
	v_mfma_f32_16x16x32_bf16 v[96:99], v[164:167], v[202:205], v[96:99]
	v_mfma_f32_16x16x32_bf16 v[96:99], v[168:171], v[206:209], v[96:99]
	v_mfma_f32_16x16x32_bf16 v[92:95], v[172:175], v[202:205], v[92:95]
	v_mfma_f32_16x16x32_bf16 v[92:95], v[176:179], v[206:209], v[92:95]
	v_mfma_f32_16x16x32_bf16 v[72:75], v[144:147], v[216:219], v[72:75]
	v_mfma_f32_16x16x32_bf16 v[72:75], v[148:151], v[220:223], v[72:75]
	v_mfma_f32_16x16x32_bf16 v[68:71], v[152:155], v[216:219], v[68:71]
	v_mfma_f32_16x16x32_bf16 v[68:71], v[156:159], v[220:223], v[68:71]
	v_mfma_f32_16x16x32_bf16 v[80:83], v[164:167], v[216:219], v[80:83]
	v_mfma_f32_16x16x32_bf16 v[80:83], v[168:171], v[220:223], v[80:83]
	v_mfma_f32_16x16x32_bf16 v[76:79], v[172:175], v[216:219], v[76:79]
	v_mfma_f32_16x16x32_bf16 v[76:79], v[176:179], v[220:223], v[76:79]
	s_barrier
; #define PG8_MMA(ai, bj, At, Bt) do { __builtin_amdgcn_s_setprio(1); _Pragma("unroll") for (int m = 0; m < 4; ++m) _Pragma("unroll") for (int n = 0; n < 2; ++n) _Pragma("unroll") for (int k = 0; k < 2; ++k) \
;         acc[ai][bj][m][n] = __builtin_amdgcn_mfma_f32_16x16x32_bf16(Bt[n][k], At[m][k], acc[ai][bj][m][n], 0, 0, 0); __builtin_amdgcn_s_setprio(0); } while (0)
; #define PG8_WAIT_V(n) asm volatile("s_waitcnt vmcnt(" #n ")" ::: "memory")
; #define PG8_TRIP_HEAD(T) const int t = (T); const bool last = (t == nt - 2); \
;             const char* a1 = cA + (size_t)(t + 1) * kstep; \
;             const char* a2 = last ? nA : cA + (size_t)(t + 2) * kstep; const char* b2 = last ? nB : cB + (size_t)(t + 2) * kstep; \
;             const char* a3 = a2 + kstep; const char* b3 = b2 + kstep; \
;             if (last && has_next) S.a_ready(nxt);
; template <class Epi, class Sched, bool ALIGN_EPI = false, bool SP2 = false>
; __device__ __forceinline__ void gemm_phase(PG8_LAS unsigned char* lds, const Gemm g, const Sched& S, const Epi& E) {
;     ...
;         if constexpr (SP2) {
;             { PG8_TRIP_HEAD(0) PG8_TRIP_SP2(asm volatile("s_waitcnt vmcnt(%0)" :: "n"(8 + Epi::NST) : "memory"), PG8_MMAZ) }
;             for (int tt = 2; tt < nt; tt += 2) { PG8_TRIP_HEAD(tt) PG8_TRIP_SP2(PG8_WAIT_V(8), PG8_MMA) }
	s_mov_b32 m0, s49
	v_lshl_add_u64 v[188:189], v[184:185], 0, s[78:79]
	ds_read_b128 v[180:183], v163 offset:49152
	ds_read_b128 v[190:193], v163 offset:50176
	ds_read_b128 v[194:197], v163 offset:51200
	ds_read_b128 v[198:201], v163 offset:52224
	ds_read_b128 v[202:205], v163 offset:53248
	ds_read_b128 v[206:209], v163 offset:54272
	ds_read_b128 v[216:219], v163 offset:55296
	ds_read_b128 v[220:223], v163 offset:56320
	global_load_lds_dwordx4 v[188:189], off
	v_lshl_add_u64 v[188:189], v[184:185], 0, s[84:85]
	s_mov_b32 m0, s50
	s_nop 0
	global_load_lds_dwordx4 v[188:189], off
	v_lshl_add_u64 v[188:189], v[184:185], 0, s[62:63]
	s_mov_b32 m0, s51
	v_lshl_add_u64 v[184:185], v[184:185], 0, s[66:67]
	global_load_lds_dwordx4 v[188:189], off
	s_mov_b32 m0, s52
	s_nop 0
	global_load_lds_dwordx4 v[184:185], off
	v_lshl_add_u64 v[184:185], v[186:187], 0, s[78:79]
	s_mov_b32 m0, s0
	s_nop 0
	global_load_lds_dwordx4 v[184:185], off
	v_lshl_add_u64 v[184:185], v[186:187], 0, s[92:93]
	s_mov_b32 m0, s41
	s_nop 0
	global_load_lds_dwordx4 v[184:185], off
	s_waitcnt vmcnt(8)
	s_waitcnt lgkmcnt(0)
	s_barrier
	v_mfma_f32_16x16x32_bf16 v[56:59], v[144:147], v[180:183], v[56:59]
	v_mfma_f32_16x16x32_bf16 v[56:59], v[148:151], v[190:193], v[56:59]
	v_mfma_f32_16x16x32_bf16 v[52:55], v[152:155], v[180:183], v[52:55]
	v_mfma_f32_16x16x32_bf16 v[52:55], v[156:159], v[190:193], v[52:55]
	v_mfma_f32_16x16x32_bf16 v[64:67], v[164:167], v[180:183], v[64:67]
	v_mfma_f32_16x16x32_bf16 v[64:67], v[168:171], v[190:193], v[64:67]
	v_mfma_f32_16x16x32_bf16 v[60:63], v[172:175], v[180:183], v[60:63]
	v_mfma_f32_16x16x32_bf16 v[60:63], v[176:179], v[190:193], v[60:63]
	v_mfma_f32_16x16x32_bf16 v[40:43], v[144:147], v[194:197], v[40:43]
	v_mfma_f32_16x16x32_bf16 v[40:43], v[148:151], v[198:201], v[40:43]
	v_mfma_f32_16x16x32_bf16 v[36:39], v[152:155], v[194:197], v[36:39]
	v_mfma_f32_16x16x32_bf16 v[36:39], v[156:159], v[198:201], v[36:39]
	v_mfma_f32_16x16x32_bf16 v[48:51], v[164:167], v[194:197], v[48:51]
	v_mfma_f32_16x16x32_bf16 v[48:51], v[168:171], v[198:201], v[48:51]
	v_mfma_f32_16x16x32_bf16 v[44:47], v[172:175], v[194:197], v[44:47]
	v_mfma_f32_16x16x32_bf16 v[44:47], v[176:179], v[198:201], v[44:47]
	v_mfma_f32_16x16x32_bf16 v[24:27], v[144:147], v[202:205], v[24:27]
	v_mfma_f32_16x16x32_bf16 v[24:27], v[148:151], v[206:209], v[24:27]
	v_mfma_f32_16x16x32_bf16 v[20:23], v[152:155], v[202:205], v[20:23]
	v_mfma_f32_16x16x32_bf16 v[20:23], v[156:159], v[206:209], v[20:23]
	v_mfma_f32_16x16x32_bf16 v[32:35], v[164:167], v[202:205], v[32:35]
	v_mfma_f32_16x16x32_bf16 v[32:35], v[168:171], v[206:209], v[32:35]
	v_mfma_f32_16x16x32_bf16 v[28:31], v[172:175], v[202:205], v[28:31]
	v_mfma_f32_16x16x32_bf16 v[28:31], v[176:179], v[206:209], v[28:31]
	v_mfma_f32_16x16x32_bf16 v[8:11], v[144:147], v[216:219], v[8:11]
	v_mfma_f32_16x16x32_bf16 v[8:11], v[148:151], v[220:223], v[8:11]
	v_mfma_f32_16x16x32_bf16 v[4:7], v[152:155], v[216:219], v[4:7]
	v_mfma_f32_16x16x32_bf16 v[4:7], v[156:159], v[220:223], v[4:7]
	v_mfma_f32_16x16x32_bf16 v[16:19], v[164:167], v[216:219], v[16:19]
	v_mfma_f32_16x16x32_bf16 v[16:19], v[168:171], v[220:223], v[16:19]
	v_mfma_f32_16x16x32_bf16 v[12:15], v[172:175], v[216:219], v[12:15]
	v_mfma_f32_16x16x32_bf16 v[12:15], v[176:179], v[220:223], v[12:15]
	s_barrier
	s_add_i32 s30, s30, 2
	s_add_u32 s10, s10, 0x100
	s_addc_u32 s11, s11, 0
	s_add_u32 s28, s28, 0x100
	s_addc_u32 s29, s29, 0
	s_cmp_gt_u32 s30, 29
	s_cbranch_scc0 .LBB0_130
	s_and_b64 vcc, exec, s[20:21]
	s_cbranch_vccz .LBB0_133
	s_barrier

.LBB0_233:
	ds_read_b128 v[120:123], v116
	ds_read_b128 v[132:135], v116 offset:1024
	ds_read_b128 v[144:147], v116 offset:2048
	ds_read_b128 v[148:151], v116 offset:3072
	ds_read_b128 v[152:155], v117
	ds_read_b128 v[156:159], v117 offset:1024
	ds_read_b128 v[166:169], v117 offset:2048
	ds_read_b128 v[170:173], v117 offset:3072
	s_add_u32 s49, s26, 0xffea0080
	s_addc_u32 s50, s27, -1
	s_cmpk_eq_i32 s48, 0x54
	s_cselect_b32 s51, s21, s50
	s_cselect_b32 s50, s20, s49
	s_cselect_b32 s53, s23, s25
	s_cselect_b32 s52, s22, s24
	s_mov_b32 m0, s0
	v_lshl_add_u64 v[188:189], s[26:27], 0, v[164:165]
	ds_read_b128 v[180:183], v178
	ds_read_b128 v[184:187], v178 offset:1024
	ds_read_b128 v[190:193], v178 offset:2048
	ds_read_b128 v[194:197], v178 offset:3072
	ds_read_b128 v[198:201], v178 offset:4096
	ds_read_b128 v[202:205], v178 offset:5120
	ds_read_b128 v[206:209], v178 offset:6144
	ds_read_b128 v[216:219], v178 offset:7168
	global_load_lds_dwordx4 v[188:189], off
	v_lshl_add_u64 v[188:189], v[188:189], 0, s[86:87]
	s_mov_b32 m0, s4
	s_nop 0
	global_load_lds_dwordx4 v[188:189], off
	s_waitcnt vmcnt(8)
	s_waitcnt lgkmcnt(0)
	s_barrier
	v_mfma_f32_16x16x32_bf16 v[140:143], v[120:123], v[180:183], v[140:143]
	v_mfma_f32_16x16x32_bf16 v[140:143], v[132:135], v[184:187], v[140:143]
	v_mfma_f32_16x16x32_bf16 v[136:139], v[144:147], v[180:183], v[136:139]
	v_mfma_f32_16x16x32_bf16 v[136:139], v[148:151], v[184:187], v[136:139]
	v_mfma_f32_16x16x32_bf16 v[128:131], v[152:155], v[180:183], v[128:131]
	v_mfma_f32_16x16x32_bf16 v[128:131], v[156:159], v[184:187], v[128:131]
	v_mfma_f32_16x16x32_bf16 v[124:127], v[166:169], v[180:183], v[124:127]
	v_mfma_f32_16x16x32_bf16 v[124:127], v[170:173], v[184:187], v[124:127]
	v_mfma_f32_16x16x32_bf16 v[112:115], v[120:123], v[190:193], v[112:115]
	v_mfma_f32_16x16x32_bf16 v[112:115], v[132:135], v[194:197], v[112:115]
	v_mfma_f32_16x16x32_bf16 v[108:111], v[144:147], v[190:193], v[108:111]
	v_mfma_f32_16x16x32_bf16 v[108:111], v[148:151], v[194:197], v[108:111]
	v_mfma_f32_16x16x32_bf16 v[104:107], v[152:155], v[190:193], v[104:107]
	v_mfma_f32_16x16x32_bf16 v[104:107], v[156:159], v[194:197], v[104:107]
	v_mfma_f32_16x16x32_bf16 v[100:103], v[166:169], v[190:193], v[100:103]
	v_mfma_f32_16x16x32_bf16 v[100:103], v[170:173], v[194:197], v[100:103]
	v_mfma_f32_16x16x32_bf16 v[96:99], v[120:123], v[198:201], v[96:99]
	v_mfma_f32_16x16x32_bf16 v[96:99], v[132:135], v[202:205], v[96:99]
	v_mfma_f32_16x16x32_bf16 v[92:95], v[144:147], v[198:201], v[92:95]
	v_mfma_f32_16x16x32_bf16 v[92:95], v[148:151], v[202:205], v[92:95]
	v_mfma_f32_16x16x32_bf16 v[88:91], v[152:155], v[198:201], v[88:91]
	v_mfma_f32_16x16x32_bf16 v[88:91], v[156:159], v[202:205], v[88:91]
	v_mfma_f32_16x16x32_bf16 v[84:87], v[166:169], v[198:201], v[84:87]
	v_mfma_f32_16x16x32_bf16 v[84:87], v[170:173], v[202:205], v[84:87]
	v_mfma_f32_16x16x32_bf16 v[80:83], v[120:123], v[206:209], v[80:83]
	v_mfma_f32_16x16x32_bf16 v[80:83], v[132:135], v[216:219], v[80:83]
	v_mfma_f32_16x16x32_bf16 v[76:79], v[144:147], v[206:209], v[76:79]
	v_mfma_f32_16x16x32_bf16 v[76:79], v[148:151], v[216:219], v[76:79]
	v_mfma_f32_16x16x32_bf16 v[72:75], v[152:155], v[206:209], v[72:75]
	v_mfma_f32_16x16x32_bf16 v[72:75], v[156:159], v[216:219], v[72:75]
	v_mfma_f32_16x16x32_bf16 v[68:71], v[166:169], v[206:209], v[68:71]
	v_mfma_f32_16x16x32_bf16 v[68:71], v[170:173], v[216:219], v[68:71]
	s_barrier
	s_mov_b32 m0, s5
	v_lshl_add_u64 v[188:189], s[52:53], 0, v[162:163]
	ds_read_b128 v[180:183], v178 offset:16384
	ds_read_b128 v[184:187], v178 offset:17408
	ds_read_b128 v[190:193], v178 offset:18432
	ds_read_b128 v[194:197], v178 offset:19456
	ds_read_b128 v[198:201], v178 offset:20480
	ds_read_b128 v[202:205], v178 offset:21504
	ds_read_b128 v[206:209], v178 offset:22528
	ds_read_b128 v[216:219], v178 offset:23552
	global_load_lds_dwordx4 v[188:189], off
	v_lshl_add_u64 v[214:215], v[188:189], 0, s[86:87]
	s_mov_b32 m0, s33
	s_nop 0
	global_load_lds_dwordx4 v[214:215], off
	v_lshl_add_u64 v[214:215], v[188:189], 0, s[54:55]
	s_mov_b32 m0, s42
	s_nop 0
	global_load_lds_dwordx4 v[214:215], off
	v_lshl_add_u64 v[214:215], v[188:189], 0, s[56:57]
	s_mov_b32 m0, s43
	s_nop 0
	global_load_lds_dwordx4 v[214:215], off
	v_lshl_add_u64 v[214:215], s[50:51], 0, v[160:161]
	s_mov_b32 m0, s31
	v_lshl_add_u64 v[220:221], v[214:215], 0, s[86:87]
	global_load_lds_dwordx4 v[214:215], off
	s_mov_b32 m0, s34
	s_nop 0
	global_load_lds_dwordx4 v[220:221], off
	s_waitcnt vmcnt(8)
	s_waitcnt lgkmcnt(0)
	s_barrier
	v_mfma_f32_16x16x32_bf16 v[56:59], v[120:123], v[180:183], v[56:59]
	v_mfma_f32_16x16x32_bf16 v[56:59], v[132:135], v[184:187], v[56:59]
	v_mfma_f32_16x16x32_bf16 v[52:55], v[144:147], v[180:183], v[52:55]
	v_mfma_f32_16x16x32_bf16 v[52:55], v[148:151], v[184:187], v[52:55]
	v_mfma_f32_16x16x32_bf16 v[64:67], v[152:155], v[180:183], v[64:67]
	v_mfma_f32_16x16x32_bf16 v[64:67], v[156:159], v[184:187], v[64:67]
	v_mfma_f32_16x16x32_bf16 v[60:63], v[166:169], v[180:183], v[60:63]
	v_mfma_f32_16x16x32_bf16 v[60:63], v[170:173], v[184:187], v[60:63]
	v_mfma_f32_16x16x32_bf16 v[48:51], v[120:123], v[190:193], v[48:51]
	v_mfma_f32_16x16x32_bf16 v[48:51], v[132:135], v[194:197], v[48:51]
	v_mfma_f32_16x16x32_bf16 v[44:47], v[144:147], v[190:193], v[44:47]
	v_mfma_f32_16x16x32_bf16 v[44:47], v[148:151], v[194:197], v[44:47]
	v_mfma_f32_16x16x32_bf16 v[40:43], v[152:155], v[190:193], v[40:43]
	v_mfma_f32_16x16x32_bf16 v[40:43], v[156:159], v[194:197], v[40:43]
	v_mfma_f32_16x16x32_bf16 v[36:39], v[166:169], v[190:193], v[36:39]
	v_mfma_f32_16x16x32_bf16 v[36:39], v[170:173], v[194:197], v[36:39]
	v_mfma_f32_16x16x32_bf16 v[32:35], v[120:123], v[198:201], v[32:35]
	v_mfma_f32_16x16x32_bf16 v[32:35], v[132:135], v[202:205], v[32:35]
	v_mfma_f32_16x16x32_bf16 v[28:31], v[144:147], v[198:201], v[28:31]
	v_mfma_f32_16x16x32_bf16 v[28:31], v[148:151], v[202:205], v[28:31]
	v_mfma_f32_16x16x32_bf16 v[24:27], v[152:155], v[198:201], v[24:27]
	v_mfma_f32_16x16x32_bf16 v[24:27], v[156:159], v[202:205], v[24:27]
	v_mfma_f32_16x16x32_bf16 v[20:23], v[166:169], v[198:201], v[20:23]
	v_mfma_f32_16x16x32_bf16 v[20:23], v[170:173], v[202:205], v[20:23]
	v_mfma_f32_16x16x32_bf16 v[16:19], v[120:123], v[206:209], v[16:19]
	v_mfma_f32_16x16x32_bf16 v[16:19], v[132:135], v[216:219], v[16:19]
	v_mfma_f32_16x16x32_bf16 v[12:15], v[144:147], v[206:209], v[12:15]
	v_mfma_f32_16x16x32_bf16 v[12:15], v[148:151], v[216:219], v[12:15]
	v_mfma_f32_16x16x32_bf16 v[8:11], v[152:155], v[206:209], v[8:11]
	v_mfma_f32_16x16x32_bf16 v[8:11], v[156:159], v[216:219], v[8:11]
	v_mfma_f32_16x16x32_bf16 v[4:7], v[166:169], v[206:209], v[4:7]
	v_mfma_f32_16x16x32_bf16 v[4:7], v[170:173], v[216:219], v[4:7]
	s_barrier
	ds_read_b128 v[120:123], v118
	ds_read_b128 v[132:135], v118 offset:1024
	ds_read_b128 v[144:147], v118 offset:2048
	ds_read_b128 v[148:151], v118 offset:3072
	ds_read_b128 v[152:155], v119
	ds_read_b128 v[156:159], v119 offset:1024
	ds_read_b128 v[166:169], v119 offset:2048
	ds_read_b128 v[170:173], v119 offset:3072
	s_mov_b32 m0, s35
	v_lshl_add_u64 v[220:221], v[214:215], 0, s[54:55]
	ds_read_b128 v[180:183], v178 offset:32768
	ds_read_b128 v[184:187], v178 offset:33792
	ds_read_b128 v[190:193], v178 offset:34816
	ds_read_b128 v[194:197], v178 offset:35840
	ds_read_b128 v[198:201], v178 offset:36864
	ds_read_b128 v[202:205], v178 offset:37888
	ds_read_b128 v[206:209], v178 offset:38912
	ds_read_b128 v[216:219], v178 offset:39936
	global_load_lds_dwordx4 v[220:221], off
	v_lshl_add_u64 v[220:221], v[214:215], 0, s[56:57]
	s_mov_b32 m0, s36
	s_nop 0
	global_load_lds_dwordx4 v[220:221], off
	s_waitcnt vmcnt(8)
	s_waitcnt lgkmcnt(0)
	s_barrier
	v_mfma_f32_16x16x32_bf16 v[140:143], v[120:123], v[180:183], v[140:143]
	v_mfma_f32_16x16x32_bf16 v[140:143], v[132:135], v[184:187], v[140:143]
	v_mfma_f32_16x16x32_bf16 v[136:139], v[144:147], v[180:183], v[136:139]
	v_mfma_f32_16x16x32_bf16 v[136:139], v[148:151], v[184:187], v[136:139]
	v_mfma_f32_16x16x32_bf16 v[128:131], v[152:155], v[180:183], v[128:131]
	v_mfma_f32_16x16x32_bf16 v[128:131], v[156:159], v[184:187], v[128:131]
	v_mfma_f32_16x16x32_bf16 v[124:127], v[166:169], v[180:183], v[124:127]
	v_mfma_f32_16x16x32_bf16 v[124:127], v[170:173], v[184:187], v[124:127]
	v_mfma_f32_16x16x32_bf16 v[112:115], v[120:123], v[190:193], v[112:115]
	v_mfma_f32_16x16x32_bf16 v[112:115], v[132:135], v[194:197], v[112:115]
	v_mfma_f32_16x16x32_bf16 v[108:111], v[144:147], v[190:193], v[108:111]
	v_mfma_f32_16x16x32_bf16 v[108:111], v[148:151], v[194:197], v[108:111]
	v_mfma_f32_16x16x32_bf16 v[104:107], v[152:155], v[190:193], v[104:107]
	v_mfma_f32_16x16x32_bf16 v[104:107], v[156:159], v[194:197], v[104:107]
	v_mfma_f32_16x16x32_bf16 v[100:103], v[166:169], v[190:193], v[100:103]
	v_mfma_f32_16x16x32_bf16 v[100:103], v[170:173], v[194:197], v[100:103]
	v_mfma_f32_16x16x32_bf16 v[96:99], v[120:123], v[198:201], v[96:99]
	v_mfma_f32_16x16x32_bf16 v[96:99], v[132:135], v[202:205], v[96:99]
	v_mfma_f32_16x16x32_bf16 v[92:95], v[144:147], v[198:201], v[92:95]
	v_mfma_f32_16x16x32_bf16 v[92:95], v[148:151], v[202:205], v[92:95]
	v_mfma_f32_16x16x32_bf16 v[88:91], v[152:155], v[198:201], v[88:91]
	v_mfma_f32_16x16x32_bf16 v[88:91], v[156:159], v[202:205], v[88:91]
	v_mfma_f32_16x16x32_bf16 v[84:87], v[166:169], v[198:201], v[84:87]
	v_mfma_f32_16x16x32_bf16 v[84:87], v[170:173], v[202:205], v[84:87]
	v_mfma_f32_16x16x32_bf16 v[80:83], v[120:123], v[206:209], v[80:83]
	v_mfma_f32_16x16x32_bf16 v[80:83], v[132:135], v[216:219], v[80:83]
	v_mfma_f32_16x16x32_bf16 v[76:79], v[144:147], v[206:209], v[76:79]
	v_mfma_f32_16x16x32_bf16 v[76:79], v[148:151], v[216:219], v[76:79]
	v_mfma_f32_16x16x32_bf16 v[72:75], v[152:155], v[206:209], v[72:75]
	v_mfma_f32_16x16x32_bf16 v[72:75], v[156:159], v[216:219], v[72:75]
	v_mfma_f32_16x16x32_bf16 v[68:71], v[166:169], v[206:209], v[68:71]
	v_mfma_f32_16x16x32_bf16 v[68:71], v[170:173], v[216:219], v[68:71]
	s_barrier
; #define PG8_MMA(ai, bj, At, Bt) do { __builtin_amdgcn_s_setprio(1); _Pragma("unroll") for (int m = 0; m < 4; ++m) _Pragma("unroll") for (int n = 0; n < 2; ++n) _Pragma("unroll") for (int k = 0; k < 2; ++k) \
;         acc[ai][bj][m][n] = __builtin_amdgcn_mfma_f32_16x16x32_bf16(Bt[n][k], At[m][k], acc[ai][bj][m][n], 0, 0, 0); __builtin_amdgcn_s_setprio(0); } while (0)
; #define PG8_WAIT_V(n) asm volatile("s_waitcnt vmcnt(" #n ")" ::: "memory")
; #define PG8_TRIP_HEAD(T) const int t = (T); const bool last = (t == nt - 2); \
;             const char* a1 = cA + (size_t)(t + 1) * kstep; \
;             const char* a2 = last ? nA : cA + (size_t)(t + 2) * kstep; const char* b2 = last ? nB : cB + (size_t)(t + 2) * kstep; \
;             const char* a3 = a2 + kstep; const char* b3 = b2 + kstep; \
;             if (last && has_next) S.a_ready(nxt);
; template <class Epi, class Sched, bool ALIGN_EPI = false, bool SP2 = false>
; __device__ __forceinline__ void gemm_phase(PG8_LAS unsigned char* lds, const Gemm g, const Sched& S, const Epi& E) {
;     ...
;         if constexpr (SP2) {
;             { PG8_TRIP_HEAD(0) PG8_TRIP_SP2(asm volatile("s_waitcnt vmcnt(%0)" :: "n"(8 + Epi::NST) : "memory"), PG8_MMAZ) }
;             for (int tt = 2; tt < nt; tt += 2) { PG8_TRIP_HEAD(tt) PG8_TRIP_SP2(PG8_WAIT_V(8), PG8_MMA) }
	s_mov_b32 m0, s44
	v_lshl_add_u64 v[220:221], v[188:189], 0, s[78:79]
	ds_read_b128 v[180:183], v178 offset:49152
	ds_read_b128 v[184:187], v178 offset:50176
	ds_read_b128 v[190:193], v178 offset:51200
	ds_read_b128 v[194:197], v178 offset:52224
	ds_read_b128 v[198:201], v178 offset:53248
	ds_read_b128 v[202:205], v178 offset:54272
	ds_read_b128 v[206:209], v178 offset:55296
	ds_read_b128 v[216:219], v178 offset:56320
	global_load_lds_dwordx4 v[220:221], off
	v_lshl_add_u64 v[220:221], v[188:189], 0, s[60:61]
	s_mov_b32 m0, s45
	s_nop 0
	global_load_lds_dwordx4 v[220:221], off
	v_lshl_add_u64 v[220:221], v[188:189], 0, s[62:63]
	s_mov_b32 m0, s46
	v_lshl_add_u64 v[188:189], v[188:189], 0, s[64:65]
	global_load_lds_dwordx4 v[220:221], off
	s_mov_b32 m0, s47
	s_nop 0
	global_load_lds_dwordx4 v[188:189], off
	v_lshl_add_u64 v[188:189], v[214:215], 0, s[78:79]
	s_mov_b32 m0, s37
	s_nop 0
	global_load_lds_dwordx4 v[188:189], off
	v_lshl_add_u64 v[188:189], v[214:215], 0, s[60:61]
	s_mov_b32 m0, s38
	s_nop 0
	global_load_lds_dwordx4 v[188:189], off
	s_waitcnt vmcnt(8)
	s_waitcnt lgkmcnt(0)
	s_barrier
	v_mfma_f32_16x16x32_bf16 v[56:59], v[120:123], v[180:183], v[56:59]
	v_mfma_f32_16x16x32_bf16 v[56:59], v[132:135], v[184:187], v[56:59]
	v_mfma_f32_16x16x32_bf16 v[52:55], v[144:147], v[180:183], v[52:55]
	v_mfma_f32_16x16x32_bf16 v[52:55], v[148:151], v[184:187], v[52:55]
	v_mfma_f32_16x16x32_bf16 v[64:67], v[152:155], v[180:183], v[64:67]
	v_mfma_f32_16x16x32_bf16 v[64:67], v[156:159], v[184:187], v[64:67]
	v_mfma_f32_16x16x32_bf16 v[60:63], v[166:169], v[180:183], v[60:63]
	v_mfma_f32_16x16x32_bf16 v[60:63], v[170:173], v[184:187], v[60:63]
	v_mfma_f32_16x16x32_bf16 v[48:51], v[120:123], v[190:193], v[48:51]
	v_mfma_f32_16x16x32_bf16 v[48:51], v[132:135], v[194:197], v[48:51]
	v_mfma_f32_16x16x32_bf16 v[44:47], v[144:147], v[190:193], v[44:47]
	v_mfma_f32_16x16x32_bf16 v[44:47], v[148:151], v[194:197], v[44:47]
	v_mfma_f32_16x16x32_bf16 v[40:43], v[152:155], v[190:193], v[40:43]
	v_mfma_f32_16x16x32_bf16 v[40:43], v[156:159], v[194:197], v[40:43]
	v_mfma_f32_16x16x32_bf16 v[36:39], v[166:169], v[190:193], v[36:39]
	v_mfma_f32_16x16x32_bf16 v[36:39], v[170:173], v[194:197], v[36:39]
	v_mfma_f32_16x16x32_bf16 v[32:35], v[120:123], v[198:201], v[32:35]
	v_mfma_f32_16x16x32_bf16 v[32:35], v[132:135], v[202:205], v[32:35]
	v_mfma_f32_16x16x32_bf16 v[28:31], v[144:147], v[198:201], v[28:31]
	v_mfma_f32_16x16x32_bf16 v[28:31], v[148:151], v[202:205], v[28:31]
	v_mfma_f32_16x16x32_bf16 v[24:27], v[152:155], v[198:201], v[24:27]
	v_mfma_f32_16x16x32_bf16 v[24:27], v[156:159], v[202:205], v[24:27]
	v_mfma_f32_16x16x32_bf16 v[20:23], v[166:169], v[198:201], v[20:23]
	v_mfma_f32_16x16x32_bf16 v[20:23], v[170:173], v[202:205], v[20:23]
	v_mfma_f32_16x16x32_bf16 v[16:19], v[120:123], v[206:209], v[16:19]
	v_mfma_f32_16x16x32_bf16 v[16:19], v[132:135], v[216:219], v[16:19]
	v_mfma_f32_16x16x32_bf16 v[12:15], v[144:147], v[206:209], v[12:15]
	v_mfma_f32_16x16x32_bf16 v[12:15], v[148:151], v[216:219], v[12:15]
	v_mfma_f32_16x16x32_bf16 v[8:11], v[152:155], v[206:209], v[8:11]
	v_mfma_f32_16x16x32_bf16 v[8:11], v[156:159], v[216:219], v[8:11]
	v_mfma_f32_16x16x32_bf16 v[4:7], v[166:169], v[206:209], v[4:7]
	v_mfma_f32_16x16x32_bf16 v[4:7], v[170:173], v[216:219], v[4:7]
	s_barrier
	s_add_i32 s48, s48, 2
	s_add_u32 s26, s26, 0x100
	s_addc_u32 s27, s27, 0
	s_add_u32 s24, s24, 0x100
	s_addc_u32 s25, s25, 0
	s_cmpk_gt_u32 s48, 0x55
	s_cbranch_scc0 .LBB0_233
	s_and_b64 vcc, exec, s[18:19]
	s_cbranch_vccz .LBB0_236
	s_barrier

.LBB0_324:
	ds_read_b128 v[136:139], v132
	ds_read_b128 v[140:143], v132 offset:1024
	ds_read_b128 v[144:147], v132 offset:2048
	ds_read_b128 v[148:151], v132 offset:3072
	ds_read_b128 v[152:155], v133
	ds_read_b128 v[156:159], v133 offset:1024
	ds_read_b128 v[160:163], v133 offset:2048
	ds_read_b128 v[174:177], v133 offset:3072
	s_add_u32 s15, s10, 0xfff7c080
	s_addc_u32 s50, s11, -1
	s_cmp_eq_u32 s14, 28
	s_cselect_b32 s51, s25, s50
	s_cselect_b32 s50, s24, s15
	s_cselect_b32 s53, s3, s13
	s_cselect_b32 s52, s4, s12
	s_mov_b32 m0, s5
	v_lshl_add_u64 v[194:195], s[10:11], 0, v[172:173]
	ds_read_b128 v[178:181], v200
	ds_read_b128 v[182:185], v200 offset:1024
	ds_read_b128 v[186:189], v200 offset:2048
	ds_read_b128 v[190:193], v200 offset:3072
	ds_read_b128 v[202:205], v200 offset:4096
	ds_read_b128 v[206:209], v200 offset:5120
	ds_read_b128 v[216:219], v200 offset:6144
	ds_read_b128 v[220:223], v200 offset:7168
	global_load_lds_dwordx4 v[194:195], off
	v_lshl_add_u64 v[194:195], v[194:195], 0, s[96:97]
	s_mov_b32 m0, s23
	s_nop 0
	global_load_lds_dwordx4 v[194:195], off
	s_waitcnt vmcnt(8)
	s_waitcnt lgkmcnt(0)
	s_barrier
	v_mfma_f32_16x16x32_bf16 v[120:123], v[136:139], v[178:181], v[120:123]
	v_mfma_f32_16x16x32_bf16 v[120:123], v[140:143], v[182:185], v[120:123]
	v_mfma_f32_16x16x32_bf16 v[116:119], v[144:147], v[178:181], v[116:119]
	v_mfma_f32_16x16x32_bf16 v[116:119], v[148:151], v[182:185], v[116:119]
	v_mfma_f32_16x16x32_bf16 v[128:131], v[152:155], v[178:181], v[128:131]
	v_mfma_f32_16x16x32_bf16 v[128:131], v[156:159], v[182:185], v[128:131]
	v_mfma_f32_16x16x32_bf16 v[124:127], v[160:163], v[178:181], v[124:127]
	v_mfma_f32_16x16x32_bf16 v[124:127], v[174:177], v[182:185], v[124:127]
	v_mfma_f32_16x16x32_bf16 v[104:107], v[136:139], v[186:189], v[104:107]
	v_mfma_f32_16x16x32_bf16 v[104:107], v[140:143], v[190:193], v[104:107]
	v_mfma_f32_16x16x32_bf16 v[100:103], v[144:147], v[186:189], v[100:103]
	v_mfma_f32_16x16x32_bf16 v[100:103], v[148:151], v[190:193], v[100:103]
	v_mfma_f32_16x16x32_bf16 v[112:115], v[152:155], v[186:189], v[112:115]
	v_mfma_f32_16x16x32_bf16 v[112:115], v[156:159], v[190:193], v[112:115]
	v_mfma_f32_16x16x32_bf16 v[108:111], v[160:163], v[186:189], v[108:111]
	v_mfma_f32_16x16x32_bf16 v[108:111], v[174:177], v[190:193], v[108:111]
	v_mfma_f32_16x16x32_bf16 v[88:91], v[136:139], v[202:205], v[88:91]
	v_mfma_f32_16x16x32_bf16 v[88:91], v[140:143], v[206:209], v[88:91]
	v_mfma_f32_16x16x32_bf16 v[84:87], v[144:147], v[202:205], v[84:87]
	v_mfma_f32_16x16x32_bf16 v[84:87], v[148:151], v[206:209], v[84:87]
	v_mfma_f32_16x16x32_bf16 v[96:99], v[152:155], v[202:205], v[96:99]
	v_mfma_f32_16x16x32_bf16 v[96:99], v[156:159], v[206:209], v[96:99]
	v_mfma_f32_16x16x32_bf16 v[92:95], v[160:163], v[202:205], v[92:95]
	v_mfma_f32_16x16x32_bf16 v[92:95], v[174:177], v[206:209], v[92:95]
	v_mfma_f32_16x16x32_bf16 v[72:75], v[136:139], v[216:219], v[72:75]
	v_mfma_f32_16x16x32_bf16 v[72:75], v[140:143], v[220:223], v[72:75]
	v_mfma_f32_16x16x32_bf16 v[68:71], v[144:147], v[216:219], v[68:71]
	v_mfma_f32_16x16x32_bf16 v[68:71], v[148:151], v[220:223], v[68:71]
	v_mfma_f32_16x16x32_bf16 v[80:83], v[152:155], v[216:219], v[80:83]
	v_mfma_f32_16x16x32_bf16 v[80:83], v[156:159], v[220:223], v[80:83]
	v_mfma_f32_16x16x32_bf16 v[76:79], v[160:163], v[216:219], v[76:79]
	v_mfma_f32_16x16x32_bf16 v[76:79], v[174:177], v[220:223], v[76:79]
	s_barrier
	s_mov_b32 m0, s28
	v_lshl_add_u64 v[194:195], s[52:53], 0, v[164:165]
	ds_read_b128 v[178:181], v200 offset:16384
	ds_read_b128 v[182:185], v200 offset:17408
	ds_read_b128 v[186:189], v200 offset:18432
	ds_read_b128 v[190:193], v200 offset:19456
	ds_read_b128 v[202:205], v200 offset:20480
	ds_read_b128 v[206:209], v200 offset:21504
	ds_read_b128 v[216:219], v200 offset:22528
	ds_read_b128 v[220:223], v200 offset:23552
	global_load_lds_dwordx4 v[194:195], off
	v_lshl_add_u64 v[214:215], v[194:195], 0, s[90:91]
	s_mov_b32 m0, s29
	s_nop 0
	global_load_lds_dwordx4 v[214:215], off
	v_lshl_add_u64 v[214:215], v[194:195], 0, s[54:55]
	s_mov_b32 m0, s33
	s_nop 0
	global_load_lds_dwordx4 v[214:215], off
	v_lshl_add_u64 v[214:215], v[194:195], 0, s[60:61]
	s_mov_b32 m0, s45
	s_nop 0
	global_load_lds_dwordx4 v[214:215], off
	v_lshl_add_u64 v[214:215], s[50:51], 0, v[166:167]
	s_mov_b32 m0, s30
	v_lshl_add_u64 v[224:225], v[214:215], 0, s[96:97]
	global_load_lds_dwordx4 v[214:215], off
	s_mov_b32 m0, s31
	s_nop 0
	global_load_lds_dwordx4 v[224:225], off
	s_waitcnt vmcnt(8)
	s_waitcnt lgkmcnt(0)
	s_barrier
	v_mfma_f32_16x16x32_bf16 v[56:59], v[136:139], v[178:181], v[56:59]
	v_mfma_f32_16x16x32_bf16 v[56:59], v[140:143], v[182:185], v[56:59]
	v_mfma_f32_16x16x32_bf16 v[52:55], v[144:147], v[178:181], v[52:55]
	v_mfma_f32_16x16x32_bf16 v[52:55], v[148:151], v[182:185], v[52:55]
	v_mfma_f32_16x16x32_bf16 v[64:67], v[152:155], v[178:181], v[64:67]
	v_mfma_f32_16x16x32_bf16 v[64:67], v[156:159], v[182:185], v[64:67]
	v_mfma_f32_16x16x32_bf16 v[60:63], v[160:163], v[178:181], v[60:63]
	v_mfma_f32_16x16x32_bf16 v[60:63], v[174:177], v[182:185], v[60:63]
	v_mfma_f32_16x16x32_bf16 v[40:43], v[136:139], v[186:189], v[40:43]
	v_mfma_f32_16x16x32_bf16 v[40:43], v[140:143], v[190:193], v[40:43]
	v_mfma_f32_16x16x32_bf16 v[36:39], v[144:147], v[186:189], v[36:39]
	v_mfma_f32_16x16x32_bf16 v[36:39], v[148:151], v[190:193], v[36:39]
	v_mfma_f32_16x16x32_bf16 v[48:51], v[152:155], v[186:189], v[48:51]
	v_mfma_f32_16x16x32_bf16 v[48:51], v[156:159], v[190:193], v[48:51]
	v_mfma_f32_16x16x32_bf16 v[44:47], v[160:163], v[186:189], v[44:47]
	v_mfma_f32_16x16x32_bf16 v[44:47], v[174:177], v[190:193], v[44:47]
	v_mfma_f32_16x16x32_bf16 v[24:27], v[136:139], v[202:205], v[24:27]
	v_mfma_f32_16x16x32_bf16 v[24:27], v[140:143], v[206:209], v[24:27]
	v_mfma_f32_16x16x32_bf16 v[20:23], v[144:147], v[202:205], v[20:23]
	v_mfma_f32_16x16x32_bf16 v[20:23], v[148:151], v[206:209], v[20:23]
	v_mfma_f32_16x16x32_bf16 v[32:35], v[152:155], v[202:205], v[32:35]
	v_mfma_f32_16x16x32_bf16 v[32:35], v[156:159], v[206:209], v[32:35]
	v_mfma_f32_16x16x32_bf16 v[28:31], v[160:163], v[202:205], v[28:31]
	v_mfma_f32_16x16x32_bf16 v[28:31], v[174:177], v[206:209], v[28:31]
	v_mfma_f32_16x16x32_bf16 v[8:11], v[136:139], v[216:219], v[8:11]
	v_mfma_f32_16x16x32_bf16 v[8:11], v[140:143], v[220:223], v[8:11]
	v_mfma_f32_16x16x32_bf16 v[4:7], v[144:147], v[216:219], v[4:7]
	v_mfma_f32_16x16x32_bf16 v[4:7], v[148:151], v[220:223], v[4:7]
	v_mfma_f32_16x16x32_bf16 v[16:19], v[152:155], v[216:219], v[16:19]
	v_mfma_f32_16x16x32_bf16 v[16:19], v[156:159], v[220:223], v[16:19]
	v_mfma_f32_16x16x32_bf16 v[12:15], v[160:163], v[216:219], v[12:15]
	v_mfma_f32_16x16x32_bf16 v[12:15], v[174:177], v[220:223], v[12:15]
	s_barrier
	ds_read_b128 v[136:139], v134
	ds_read_b128 v[140:143], v134 offset:1024
	ds_read_b128 v[144:147], v134 offset:2048
	ds_read_b128 v[148:151], v134 offset:3072
	ds_read_b128 v[152:155], v135
	ds_read_b128 v[156:159], v135 offset:1024
	ds_read_b128 v[160:163], v135 offset:2048
	ds_read_b128 v[174:177], v135 offset:3072
	s_mov_b32 m0, s34
	v_lshl_add_u64 v[224:225], v[214:215], 0, s[82:83]
	ds_read_b128 v[178:181], v200 offset:32768
	ds_read_b128 v[182:185], v200 offset:33792
	ds_read_b128 v[186:189], v200 offset:34816
	ds_read_b128 v[190:193], v200 offset:35840
	ds_read_b128 v[202:205], v200 offset:36864
	ds_read_b128 v[206:209], v200 offset:37888
	ds_read_b128 v[216:219], v200 offset:38912
	ds_read_b128 v[220:223], v200 offset:39936
	global_load_lds_dwordx4 v[224:225], off
	v_lshl_add_u64 v[224:225], v[214:215], 0, s[64:65]
	s_mov_b32 m0, s35
	s_nop 0
	global_load_lds_dwordx4 v[224:225], off
	s_waitcnt vmcnt(8)
	s_waitcnt lgkmcnt(0)
	s_barrier
	v_mfma_f32_16x16x32_bf16 v[120:123], v[136:139], v[178:181], v[120:123]
	v_mfma_f32_16x16x32_bf16 v[120:123], v[140:143], v[182:185], v[120:123]
	v_mfma_f32_16x16x32_bf16 v[116:119], v[144:147], v[178:181], v[116:119]
	v_mfma_f32_16x16x32_bf16 v[116:119], v[148:151], v[182:185], v[116:119]
	v_mfma_f32_16x16x32_bf16 v[128:131], v[152:155], v[178:181], v[128:131]
	v_mfma_f32_16x16x32_bf16 v[128:131], v[156:159], v[182:185], v[128:131]
	v_mfma_f32_16x16x32_bf16 v[124:127], v[160:163], v[178:181], v[124:127]
	v_mfma_f32_16x16x32_bf16 v[124:127], v[174:177], v[182:185], v[124:127]
	v_mfma_f32_16x16x32_bf16 v[104:107], v[136:139], v[186:189], v[104:107]
	v_mfma_f32_16x16x32_bf16 v[104:107], v[140:143], v[190:193], v[104:107]
	v_mfma_f32_16x16x32_bf16 v[100:103], v[144:147], v[186:189], v[100:103]
	v_mfma_f32_16x16x32_bf16 v[100:103], v[148:151], v[190:193], v[100:103]
	v_mfma_f32_16x16x32_bf16 v[112:115], v[152:155], v[186:189], v[112:115]
	v_mfma_f32_16x16x32_bf16 v[112:115], v[156:159], v[190:193], v[112:115]
	v_mfma_f32_16x16x32_bf16 v[108:111], v[160:163], v[186:189], v[108:111]
	v_mfma_f32_16x16x32_bf16 v[108:111], v[174:177], v[190:193], v[108:111]
	v_mfma_f32_16x16x32_bf16 v[88:91], v[136:139], v[202:205], v[88:91]
	v_mfma_f32_16x16x32_bf16 v[88:91], v[140:143], v[206:209], v[88:91]
	v_mfma_f32_16x16x32_bf16 v[84:87], v[144:147], v[202:205], v[84:87]
	v_mfma_f32_16x16x32_bf16 v[84:87], v[148:151], v[206:209], v[84:87]
	v_mfma_f32_16x16x32_bf16 v[96:99], v[152:155], v[202:205], v[96:99]
	v_mfma_f32_16x16x32_bf16 v[96:99], v[156:159], v[206:209], v[96:99]
	v_mfma_f32_16x16x32_bf16 v[92:95], v[160:163], v[202:205], v[92:95]
	v_mfma_f32_16x16x32_bf16 v[92:95], v[174:177], v[206:209], v[92:95]
	v_mfma_f32_16x16x32_bf16 v[72:75], v[136:139], v[216:219], v[72:75]
	v_mfma_f32_16x16x32_bf16 v[72:75], v[140:143], v[220:223], v[72:75]
	v_mfma_f32_16x16x32_bf16 v[68:71], v[144:147], v[216:219], v[68:71]
	v_mfma_f32_16x16x32_bf16 v[68:71], v[148:151], v[220:223], v[68:71]
	v_mfma_f32_16x16x32_bf16 v[80:83], v[152:155], v[216:219], v[80:83]
	v_mfma_f32_16x16x32_bf16 v[80:83], v[156:159], v[220:223], v[80:83]
	v_mfma_f32_16x16x32_bf16 v[76:79], v[160:163], v[216:219], v[76:79]
	v_mfma_f32_16x16x32_bf16 v[76:79], v[174:177], v[220:223], v[76:79]
	s_barrier
; #define PG8_MMA(ai, bj, At, Bt) do { __builtin_amdgcn_s_setprio(1); _Pragma("unroll") for (int m = 0; m < 4; ++m) _Pragma("unroll") for (int n = 0; n < 2; ++n) _Pragma("unroll") for (int k = 0; k < 2; ++k) \
;         acc[ai][bj][m][n] = __builtin_amdgcn_mfma_f32_16x16x32_bf16(Bt[n][k], At[m][k], acc[ai][bj][m][n], 0, 0, 0); __builtin_amdgcn_s_setprio(0); } while (0)
; #define PG8_WAIT_V(n) asm volatile("s_waitcnt vmcnt(" #n ")" ::: "memory")
; #define PG8_TRIP_HEAD(T) const int t = (T); const bool last = (t == nt - 2); \
;             const char* a1 = cA + (size_t)(t + 1) * kstep; \
;             const char* a2 = last ? nA : cA + (size_t)(t + 2) * kstep; const char* b2 = last ? nB : cB + (size_t)(t + 2) * kstep; \
;             const char* a3 = a2 + kstep; const char* b3 = b2 + kstep; \
;             if (last && has_next) S.a_ready(nxt);
; template <class Epi, class Sched, bool ALIGN_EPI = false, bool SP2 = false>
; __device__ __forceinline__ void gemm_phase(PG8_LAS unsigned char* lds, const Gemm g, const Sched& S, const Epi& E) {
;     ...
;         if constexpr (SP2) {
;             { PG8_TRIP_HEAD(0) PG8_TRIP_SP2(asm volatile("s_waitcnt vmcnt(%0)" :: "n"(8 + Epi::NST) : "memory"), PG8_MMAZ) }
;             for (int tt = 2; tt < nt; tt += 2) { PG8_TRIP_HEAD(tt) PG8_TRIP_SP2(PG8_WAIT_V(8), PG8_MMA) }
	s_mov_b32 m0, s46
	v_lshl_add_u64 v[224:225], v[194:195], 0, s[78:79]
	ds_read_b128 v[178:181], v200 offset:49152
	ds_read_b128 v[182:185], v200 offset:50176
	ds_read_b128 v[186:189], v200 offset:51200
	ds_read_b128 v[190:193], v200 offset:52224
	ds_read_b128 v[202:205], v200 offset:53248
	ds_read_b128 v[206:209], v200 offset:54272
	ds_read_b128 v[216:219], v200 offset:55296
	ds_read_b128 v[220:223], v200 offset:56320
	global_load_lds_dwordx4 v[224:225], off
	v_lshl_add_u64 v[224:225], v[194:195], 0, s[84:85]
	s_mov_b32 m0, s47
	s_nop 0
	global_load_lds_dwordx4 v[224:225], off
	v_lshl_add_u64 v[224:225], v[194:195], 0, s[56:57]
	s_mov_b32 m0, s48
	v_lshl_add_u64 v[194:195], v[194:195], 0, s[62:63]
	global_load_lds_dwordx4 v[224:225], off
	s_mov_b32 m0, s49
	s_nop 0
	global_load_lds_dwordx4 v[194:195], off
	v_lshl_add_u64 v[194:195], v[214:215], 0, s[78:79]
	s_mov_b32 m0, s38
	s_nop 0
	global_load_lds_dwordx4 v[194:195], off
	v_lshl_add_u64 v[194:195], v[214:215], 0, s[92:93]
	s_mov_b32 m0, s39
	s_nop 0
	global_load_lds_dwordx4 v[194:195], off
	s_waitcnt vmcnt(8)
	s_waitcnt lgkmcnt(0)
	s_barrier
	v_mfma_f32_16x16x32_bf16 v[56:59], v[136:139], v[178:181], v[56:59]
	v_mfma_f32_16x16x32_bf16 v[56:59], v[140:143], v[182:185], v[56:59]
	v_mfma_f32_16x16x32_bf16 v[52:55], v[144:147], v[178:181], v[52:55]
	v_mfma_f32_16x16x32_bf16 v[52:55], v[148:151], v[182:185], v[52:55]
	v_mfma_f32_16x16x32_bf16 v[64:67], v[152:155], v[178:181], v[64:67]
	v_mfma_f32_16x16x32_bf16 v[64:67], v[156:159], v[182:185], v[64:67]
	v_mfma_f32_16x16x32_bf16 v[60:63], v[160:163], v[178:181], v[60:63]
	v_mfma_f32_16x16x32_bf16 v[60:63], v[174:177], v[182:185], v[60:63]
	v_mfma_f32_16x16x32_bf16 v[40:43], v[136:139], v[186:189], v[40:43]
	v_mfma_f32_16x16x32_bf16 v[40:43], v[140:143], v[190:193], v[40:43]
	v_mfma_f32_16x16x32_bf16 v[36:39], v[144:147], v[186:189], v[36:39]
	v_mfma_f32_16x16x32_bf16 v[36:39], v[148:151], v[190:193], v[36:39]
	v_mfma_f32_16x16x32_bf16 v[48:51], v[152:155], v[186:189], v[48:51]
	v_mfma_f32_16x16x32_bf16 v[48:51], v[156:159], v[190:193], v[48:51]
	v_mfma_f32_16x16x32_bf16 v[44:47], v[160:163], v[186:189], v[44:47]
	v_mfma_f32_16x16x32_bf16 v[44:47], v[174:177], v[190:193], v[44:47]
	v_mfma_f32_16x16x32_bf16 v[24:27], v[136:139], v[202:205], v[24:27]
	v_mfma_f32_16x16x32_bf16 v[24:27], v[140:143], v[206:209], v[24:27]
	v_mfma_f32_16x16x32_bf16 v[20:23], v[144:147], v[202:205], v[20:23]
	v_mfma_f32_16x16x32_bf16 v[20:23], v[148:151], v[206:209], v[20:23]
	v_mfma_f32_16x16x32_bf16 v[32:35], v[152:155], v[202:205], v[32:35]
	v_mfma_f32_16x16x32_bf16 v[32:35], v[156:159], v[206:209], v[32:35]
	v_mfma_f32_16x16x32_bf16 v[28:31], v[160:163], v[202:205], v[28:31]
	v_mfma_f32_16x16x32_bf16 v[28:31], v[174:177], v[206:209], v[28:31]
	v_mfma_f32_16x16x32_bf16 v[8:11], v[136:139], v[216:219], v[8:11]
	v_mfma_f32_16x16x32_bf16 v[8:11], v[140:143], v[220:223], v[8:11]
	v_mfma_f32_16x16x32_bf16 v[4:7], v[144:147], v[216:219], v[4:7]
	v_mfma_f32_16x16x32_bf16 v[4:7], v[148:151], v[220:223], v[4:7]
	v_mfma_f32_16x16x32_bf16 v[16:19], v[152:155], v[216:219], v[16:19]
	v_mfma_f32_16x16x32_bf16 v[16:19], v[156:159], v[220:223], v[16:19]
	v_mfma_f32_16x16x32_bf16 v[12:15], v[160:163], v[216:219], v[12:15]
	v_mfma_f32_16x16x32_bf16 v[12:15], v[174:177], v[220:223], v[12:15]
	s_barrier
	s_add_i32 s14, s14, 2
	s_add_u32 s10, s10, 0x100
	s_addc_u32 s11, s11, 0
	s_add_u32 s12, s12, 0x100
	s_addc_u32 s13, s13, 0
	s_cmp_gt_u32 s14, 29
	s_cbranch_scc0 .LBB0_324
	s_and_b64 vcc, exec, s[18:19]
	s_cbranch_vccz .LBB0_327
	s_barrier

.LBB0_594:
	ds_read_b128 v[136:139], v116
	ds_read_b128 v[140:143], v116 offset:1024
	ds_read_b128 v[144:147], v116 offset:2048
	ds_read_b128 v[148:151], v116 offset:3072
	ds_read_b128 v[152:155], v117
	ds_read_b128 v[156:159], v117 offset:1024
	ds_read_b128 v[160:163], v117 offset:2048
	ds_read_b128 v[164:167], v117 offset:3072
	s_add_u32 s43, s20, 0xfff7c080
	s_addc_u32 s44, s21, -1
	s_cmp_eq_u32 s15, 28
	s_cselect_b32 s45, s17, s44
	s_cselect_b32 s44, s16, s43
	s_cselect_b32 s47, s4, s9
	s_cselect_b32 s46, s5, s8
	s_mov_b32 m0, s33
	v_lshl_add_u64 v[192:193], s[20:21], 0, v[200:201]
	ds_read_b128 v[168:171], v221
	ds_read_b128 v[172:175], v221 offset:1024
	ds_read_b128 v[176:179], v221 offset:2048
	ds_read_b128 v[180:183], v221 offset:3072
	ds_read_b128 v[184:187], v221 offset:4096
	ds_read_b128 v[188:191], v221 offset:5120
	ds_read_b128 v[202:205], v221 offset:6144
	ds_read_b128 v[206:209], v221 offset:7168
	global_load_lds_dwordx4 v[192:193], off
	v_lshl_add_u64 v[192:193], v[192:193], 0, s[96:97]
	s_mov_b32 m0, s34
	s_nop 0
	global_load_lds_dwordx4 v[192:193], off
	s_waitcnt vmcnt(8)
	s_waitcnt lgkmcnt(0)
	s_barrier
	v_mfma_f32_16x16x32_bf16 v[130:133], v[136:139], v[168:171], v[130:133]
	v_mfma_f32_16x16x32_bf16 v[130:133], v[140:143], v[172:175], v[130:133]
	v_mfma_f32_16x16x32_bf16 v[126:129], v[144:147], v[168:171], v[126:129]
	v_mfma_f32_16x16x32_bf16 v[126:129], v[148:151], v[172:175], v[126:129]
	v_mfma_f32_16x16x32_bf16 v[122:125], v[152:155], v[168:171], v[122:125]
	v_mfma_f32_16x16x32_bf16 v[122:125], v[156:159], v[172:175], v[122:125]
	v_mfma_f32_16x16x32_bf16 v[118:121], v[160:163], v[168:171], v[118:121]
	v_mfma_f32_16x16x32_bf16 v[118:121], v[164:167], v[172:175], v[118:121]
	v_mfma_f32_16x16x32_bf16 v[112:115], v[136:139], v[176:179], v[112:115]
	v_mfma_f32_16x16x32_bf16 v[112:115], v[140:143], v[180:183], v[112:115]
	v_mfma_f32_16x16x32_bf16 v[108:111], v[144:147], v[176:179], v[108:111]
	v_mfma_f32_16x16x32_bf16 v[108:111], v[148:151], v[180:183], v[108:111]
	v_mfma_f32_16x16x32_bf16 v[104:107], v[152:155], v[176:179], v[104:107]
	v_mfma_f32_16x16x32_bf16 v[104:107], v[156:159], v[180:183], v[104:107]
	v_mfma_f32_16x16x32_bf16 v[100:103], v[160:163], v[176:179], v[100:103]
	v_mfma_f32_16x16x32_bf16 v[100:103], v[164:167], v[180:183], v[100:103]
	v_mfma_f32_16x16x32_bf16 v[96:99], v[136:139], v[184:187], v[96:99]
	v_mfma_f32_16x16x32_bf16 v[96:99], v[140:143], v[188:191], v[96:99]
	v_mfma_f32_16x16x32_bf16 v[92:95], v[144:147], v[184:187], v[92:95]
	v_mfma_f32_16x16x32_bf16 v[92:95], v[148:151], v[188:191], v[92:95]
	v_mfma_f32_16x16x32_bf16 v[88:91], v[152:155], v[184:187], v[88:91]
	v_mfma_f32_16x16x32_bf16 v[88:91], v[156:159], v[188:191], v[88:91]
	v_mfma_f32_16x16x32_bf16 v[84:87], v[160:163], v[184:187], v[84:87]
	v_mfma_f32_16x16x32_bf16 v[84:87], v[164:167], v[188:191], v[84:87]
	v_mfma_f32_16x16x32_bf16 v[80:83], v[136:139], v[202:205], v[80:83]
	v_mfma_f32_16x16x32_bf16 v[80:83], v[140:143], v[206:209], v[80:83]
	v_mfma_f32_16x16x32_bf16 v[76:79], v[144:147], v[202:205], v[76:79]
	v_mfma_f32_16x16x32_bf16 v[76:79], v[148:151], v[206:209], v[76:79]
	v_mfma_f32_16x16x32_bf16 v[72:75], v[152:155], v[202:205], v[72:75]
	v_mfma_f32_16x16x32_bf16 v[72:75], v[156:159], v[206:209], v[72:75]
	v_mfma_f32_16x16x32_bf16 v[68:71], v[160:163], v[202:205], v[68:71]
	v_mfma_f32_16x16x32_bf16 v[68:71], v[164:167], v[206:209], v[68:71]
	s_barrier
	s_mov_b32 m0, s35
	v_lshl_add_u64 v[192:193], s[46:47], 0, v[194:195]
	ds_read_b128 v[168:171], v221 offset:16384
	ds_read_b128 v[172:175], v221 offset:17408
	ds_read_b128 v[176:179], v221 offset:18432
	ds_read_b128 v[180:183], v221 offset:19456
	ds_read_b128 v[184:187], v221 offset:20480
	ds_read_b128 v[188:191], v221 offset:21504
	ds_read_b128 v[202:205], v221 offset:22528
	ds_read_b128 v[206:209], v221 offset:23552
	global_load_lds_dwordx4 v[192:193], off
	v_lshl_add_u64 v[214:215], v[192:193], 0, s[90:91]
	s_mov_b32 m0, s36
	s_nop 0
	global_load_lds_dwordx4 v[214:215], off
	v_lshl_add_u64 v[214:215], v[192:193], 0, s[48:49]
	s_mov_b32 m0, s37
	s_nop 0
	global_load_lds_dwordx4 v[214:215], off
	v_lshl_add_u64 v[214:215], v[192:193], 0, s[52:53]
	s_mov_b32 m0, s38
	s_nop 0
	global_load_lds_dwordx4 v[214:215], off
	v_lshl_add_u64 v[214:215], s[44:45], 0, v[196:197]
	s_mov_b32 m0, s23
	v_lshl_add_u64 v[216:217], v[214:215], 0, s[96:97]
	global_load_lds_dwordx4 v[214:215], off
	s_mov_b32 m0, s24
	s_nop 0
	global_load_lds_dwordx4 v[216:217], off
	s_waitcnt vmcnt(8)
	s_waitcnt lgkmcnt(0)
	s_barrier
	v_mfma_f32_16x16x32_bf16 v[64:67], v[136:139], v[168:171], v[64:67]
	v_mfma_f32_16x16x32_bf16 v[64:67], v[140:143], v[172:175], v[64:67]
	v_mfma_f32_16x16x32_bf16 v[60:63], v[144:147], v[168:171], v[60:63]
	v_mfma_f32_16x16x32_bf16 v[60:63], v[148:151], v[172:175], v[60:63]
	v_mfma_f32_16x16x32_bf16 v[56:59], v[152:155], v[168:171], v[56:59]
	v_mfma_f32_16x16x32_bf16 v[56:59], v[156:159], v[172:175], v[56:59]
	v_mfma_f32_16x16x32_bf16 v[52:55], v[160:163], v[168:171], v[52:55]
	v_mfma_f32_16x16x32_bf16 v[52:55], v[164:167], v[172:175], v[52:55]
	v_mfma_f32_16x16x32_bf16 v[48:51], v[136:139], v[176:179], v[48:51]
	v_mfma_f32_16x16x32_bf16 v[48:51], v[140:143], v[180:183], v[48:51]
	v_mfma_f32_16x16x32_bf16 v[44:47], v[144:147], v[176:179], v[44:47]
	v_mfma_f32_16x16x32_bf16 v[44:47], v[148:151], v[180:183], v[44:47]
	v_mfma_f32_16x16x32_bf16 v[40:43], v[152:155], v[176:179], v[40:43]
	v_mfma_f32_16x16x32_bf16 v[40:43], v[156:159], v[180:183], v[40:43]
	v_mfma_f32_16x16x32_bf16 v[36:39], v[160:163], v[176:179], v[36:39]
	v_mfma_f32_16x16x32_bf16 v[36:39], v[164:167], v[180:183], v[36:39]
	v_mfma_f32_16x16x32_bf16 v[32:35], v[136:139], v[184:187], v[32:35]
	v_mfma_f32_16x16x32_bf16 v[32:35], v[140:143], v[188:191], v[32:35]
	v_mfma_f32_16x16x32_bf16 v[28:31], v[144:147], v[184:187], v[28:31]
	v_mfma_f32_16x16x32_bf16 v[28:31], v[148:151], v[188:191], v[28:31]
	v_mfma_f32_16x16x32_bf16 v[24:27], v[152:155], v[184:187], v[24:27]
	v_mfma_f32_16x16x32_bf16 v[24:27], v[156:159], v[188:191], v[24:27]
	v_mfma_f32_16x16x32_bf16 v[20:23], v[160:163], v[184:187], v[20:23]
	v_mfma_f32_16x16x32_bf16 v[20:23], v[164:167], v[188:191], v[20:23]
	v_mfma_f32_16x16x32_bf16 v[16:19], v[136:139], v[202:205], v[16:19]
	v_mfma_f32_16x16x32_bf16 v[16:19], v[140:143], v[206:209], v[16:19]
	v_mfma_f32_16x16x32_bf16 v[12:15], v[144:147], v[202:205], v[12:15]
	v_mfma_f32_16x16x32_bf16 v[12:15], v[148:151], v[206:209], v[12:15]
	v_mfma_f32_16x16x32_bf16 v[8:11], v[152:155], v[202:205], v[8:11]
	v_mfma_f32_16x16x32_bf16 v[8:11], v[156:159], v[206:209], v[8:11]
	v_mfma_f32_16x16x32_bf16 v[4:7], v[160:163], v[202:205], v[4:7]
	v_mfma_f32_16x16x32_bf16 v[4:7], v[164:167], v[206:209], v[4:7]
	s_barrier
; #define PG8_MMA(ai, bj, At, Bt) do { __builtin_amdgcn_s_setprio(1); _Pragma("unroll") for (int m = 0; m < 4; ++m) _Pragma("unroll") for (int n = 0; n < 2; ++n) _Pragma("unroll") for (int k = 0; k < 2; ++k) \
;         acc[ai][bj][m][n] = __builtin_amdgcn_mfma_f32_16x16x32_bf16(Bt[n][k], At[m][k], acc[ai][bj][m][n], 0, 0, 0); __builtin_amdgcn_s_setprio(0); } while (0)
; #define PG8_WAIT_V(n) asm volatile("s_waitcnt vmcnt(" #n ")" ::: "memory")
; #define PG8_TRIP_HEAD(T) const int t = (T); const bool last = (t == nt - 2); \
;             const char* a1 = cA + (size_t)(t + 1) * kstep; \
;             const char* a2 = last ? nA : cA + (size_t)(t + 2) * kstep; const char* b2 = last ? nB : cB + (size_t)(t + 2) * kstep; \
;             const char* a3 = a2 + kstep; const char* b3 = b2 + kstep; \
;             if (last && has_next) S.a_ready(nxt);
; template <class Epi, class Sched, bool ALIGN_EPI = false, bool SP2 = false>
; __device__ __forceinline__ void gemm_phase(PG8_LAS unsigned char* lds, const Gemm g, const Sched& S, const Epi& E) {
;     ...
;         if constexpr (SP2) {
;             { PG8_TRIP_HEAD(0) PG8_TRIP_SP2(asm volatile("s_waitcnt vmcnt(%0)" :: "n"(8 + Epi::NST) : "memory"), PG8_MMAZ) }
;             for (int tt = 2; tt < nt; tt += 2) { PG8_TRIP_HEAD(tt) PG8_TRIP_SP2(PG8_WAIT_V(8), PG8_MMA) }
	ds_read_b128 v[136:139], v134
	ds_read_b128 v[140:143], v134 offset:1024
	ds_read_b128 v[144:147], v134 offset:2048
	ds_read_b128 v[148:151], v134 offset:3072
	ds_read_b128 v[152:155], v135
	ds_read_b128 v[156:159], v135 offset:1024
	ds_read_b128 v[160:163], v135 offset:2048
	ds_read_b128 v[164:167], v135 offset:3072
	s_mov_b32 m0, s25
	v_lshl_add_u64 v[216:217], v[214:215], 0, s[82:83]
	ds_read_b128 v[168:171], v221 offset:32768
	ds_read_b128 v[172:175], v221 offset:33792
	ds_read_b128 v[176:179], v221 offset:34816
	ds_read_b128 v[180:183], v221 offset:35840
	ds_read_b128 v[184:187], v221 offset:36864
	ds_read_b128 v[188:191], v221 offset:37888
	ds_read_b128 v[202:205], v221 offset:38912
	ds_read_b128 v[206:209], v221 offset:39936
	global_load_lds_dwordx4 v[216:217], off
	v_lshl_add_u64 v[216:217], v[214:215], 0, s[56:57]
	s_mov_b32 m0, s26
	s_nop 0
	global_load_lds_dwordx4 v[216:217], off
	s_waitcnt vmcnt(8)
	s_waitcnt lgkmcnt(0)
	s_barrier
	v_mfma_f32_16x16x32_bf16 v[130:133], v[136:139], v[168:171], v[130:133]
	v_mfma_f32_16x16x32_bf16 v[130:133], v[140:143], v[172:175], v[130:133]
	v_mfma_f32_16x16x32_bf16 v[126:129], v[144:147], v[168:171], v[126:129]
	v_mfma_f32_16x16x32_bf16 v[126:129], v[148:151], v[172:175], v[126:129]
	v_mfma_f32_16x16x32_bf16 v[122:125], v[152:155], v[168:171], v[122:125]
	v_mfma_f32_16x16x32_bf16 v[122:125], v[156:159], v[172:175], v[122:125]
	v_mfma_f32_16x16x32_bf16 v[118:121], v[160:163], v[168:171], v[118:121]
	v_mfma_f32_16x16x32_bf16 v[118:121], v[164:167], v[172:175], v[118:121]
	v_mfma_f32_16x16x32_bf16 v[112:115], v[136:139], v[176:179], v[112:115]
	v_mfma_f32_16x16x32_bf16 v[112:115], v[140:143], v[180:183], v[112:115]
	v_mfma_f32_16x16x32_bf16 v[108:111], v[144:147], v[176:179], v[108:111]
	v_mfma_f32_16x16x32_bf16 v[108:111], v[148:151], v[180:183], v[108:111]
	v_mfma_f32_16x16x32_bf16 v[104:107], v[152:155], v[176:179], v[104:107]
	v_mfma_f32_16x16x32_bf16 v[104:107], v[156:159], v[180:183], v[104:107]
	v_mfma_f32_16x16x32_bf16 v[100:103], v[160:163], v[176:179], v[100:103]
	v_mfma_f32_16x16x32_bf16 v[100:103], v[164:167], v[180:183], v[100:103]
	v_mfma_f32_16x16x32_bf16 v[96:99], v[136:139], v[184:187], v[96:99]
	v_mfma_f32_16x16x32_bf16 v[96:99], v[140:143], v[188:191], v[96:99]
	v_mfma_f32_16x16x32_bf16 v[92:95], v[144:147], v[184:187], v[92:95]
	v_mfma_f32_16x16x32_bf16 v[92:95], v[148:151], v[188:191], v[92:95]
	v_mfma_f32_16x16x32_bf16 v[88:91], v[152:155], v[184:187], v[88:91]
	v_mfma_f32_16x16x32_bf16 v[88:91], v[156:159], v[188:191], v[88:91]
	v_mfma_f32_16x16x32_bf16 v[84:87], v[160:163], v[184:187], v[84:87]
	v_mfma_f32_16x16x32_bf16 v[84:87], v[164:167], v[188:191], v[84:87]
	v_mfma_f32_16x16x32_bf16 v[80:83], v[136:139], v[202:205], v[80:83]
	v_mfma_f32_16x16x32_bf16 v[80:83], v[140:143], v[206:209], v[80:83]
	v_mfma_f32_16x16x32_bf16 v[76:79], v[144:147], v[202:205], v[76:79]
	v_mfma_f32_16x16x32_bf16 v[76:79], v[148:151], v[206:209], v[76:79]
	v_mfma_f32_16x16x32_bf16 v[72:75], v[152:155], v[202:205], v[72:75]
	v_mfma_f32_16x16x32_bf16 v[72:75], v[156:159], v[206:209], v[72:75]
	v_mfma_f32_16x16x32_bf16 v[68:71], v[160:163], v[202:205], v[68:71]
	v_mfma_f32_16x16x32_bf16 v[68:71], v[164:167], v[206:209], v[68:71]
	s_barrier
	s_mov_b32 m0, s39
	v_lshl_add_u64 v[216:217], v[192:193], 0, s[78:79]
	ds_read_b128 v[168:171], v221 offset:49152
	ds_read_b128 v[172:175], v221 offset:50176
	ds_read_b128 v[176:179], v221 offset:51200
	ds_read_b128 v[180:183], v221 offset:52224
	ds_read_b128 v[184:187], v221 offset:53248
	ds_read_b128 v[188:191], v221 offset:54272
	ds_read_b128 v[202:205], v221 offset:55296
	ds_read_b128 v[206:209], v221 offset:56320
	global_load_lds_dwordx4 v[216:217], off
	v_lshl_add_u64 v[216:217], v[192:193], 0, s[84:85]
	s_mov_b32 m0, s40
	s_nop 0
	global_load_lds_dwordx4 v[216:217], off
	v_lshl_add_u64 v[216:217], v[192:193], 0, s[50:51]
	s_mov_b32 m0, s41
	v_lshl_add_u64 v[192:193], v[192:193], 0, s[54:55]
	global_load_lds_dwordx4 v[216:217], off
	s_mov_b32 m0, s42
	s_nop 0
	global_load_lds_dwordx4 v[192:193], off
	v_lshl_add_u64 v[192:193], v[214:215], 0, s[78:79]
	s_mov_b32 m0, s27
	s_nop 0
	global_load_lds_dwordx4 v[192:193], off
	v_lshl_add_u64 v[192:193], v[214:215], 0, s[92:93]
	s_mov_b32 m0, s28
	s_nop 0
	global_load_lds_dwordx4 v[192:193], off
	s_waitcnt vmcnt(8)
	s_waitcnt lgkmcnt(0)
	s_barrier
	v_mfma_f32_16x16x32_bf16 v[64:67], v[136:139], v[168:171], v[64:67]
	v_mfma_f32_16x16x32_bf16 v[64:67], v[140:143], v[172:175], v[64:67]
	v_mfma_f32_16x16x32_bf16 v[60:63], v[144:147], v[168:171], v[60:63]
	v_mfma_f32_16x16x32_bf16 v[60:63], v[148:151], v[172:175], v[60:63]
	v_mfma_f32_16x16x32_bf16 v[56:59], v[152:155], v[168:171], v[56:59]
	v_mfma_f32_16x16x32_bf16 v[56:59], v[156:159], v[172:175], v[56:59]
	v_mfma_f32_16x16x32_bf16 v[52:55], v[160:163], v[168:171], v[52:55]
	v_mfma_f32_16x16x32_bf16 v[52:55], v[164:167], v[172:175], v[52:55]
	v_mfma_f32_16x16x32_bf16 v[48:51], v[136:139], v[176:179], v[48:51]
	v_mfma_f32_16x16x32_bf16 v[48:51], v[140:143], v[180:183], v[48:51]
	v_mfma_f32_16x16x32_bf16 v[44:47], v[144:147], v[176:179], v[44:47]
	v_mfma_f32_16x16x32_bf16 v[44:47], v[148:151], v[180:183], v[44:47]
	v_mfma_f32_16x16x32_bf16 v[40:43], v[152:155], v[176:179], v[40:43]
	v_mfma_f32_16x16x32_bf16 v[40:43], v[156:159], v[180:183], v[40:43]
	v_mfma_f32_16x16x32_bf16 v[36:39], v[160:163], v[176:179], v[36:39]
	v_mfma_f32_16x16x32_bf16 v[36:39], v[164:167], v[180:183], v[36:39]
	v_mfma_f32_16x16x32_bf16 v[32:35], v[136:139], v[184:187], v[32:35]
	v_mfma_f32_16x16x32_bf16 v[32:35], v[140:143], v[188:191], v[32:35]
	v_mfma_f32_16x16x32_bf16 v[28:31], v[144:147], v[184:187], v[28:31]
	v_mfma_f32_16x16x32_bf16 v[28:31], v[148:151], v[188:191], v[28:31]
	v_mfma_f32_16x16x32_bf16 v[24:27], v[152:155], v[184:187], v[24:27]
	v_mfma_f32_16x16x32_bf16 v[24:27], v[156:159], v[188:191], v[24:27]
	v_mfma_f32_16x16x32_bf16 v[20:23], v[160:163], v[184:187], v[20:23]
	v_mfma_f32_16x16x32_bf16 v[20:23], v[164:167], v[188:191], v[20:23]
	v_mfma_f32_16x16x32_bf16 v[16:19], v[136:139], v[202:205], v[16:19]
	v_mfma_f32_16x16x32_bf16 v[16:19], v[140:143], v[206:209], v[16:19]
	v_mfma_f32_16x16x32_bf16 v[12:15], v[144:147], v[202:205], v[12:15]
	v_mfma_f32_16x16x32_bf16 v[12:15], v[148:151], v[206:209], v[12:15]
	v_mfma_f32_16x16x32_bf16 v[8:11], v[152:155], v[202:205], v[8:11]
	v_mfma_f32_16x16x32_bf16 v[8:11], v[156:159], v[206:209], v[8:11]
	v_mfma_f32_16x16x32_bf16 v[4:7], v[160:163], v[202:205], v[4:7]
	v_mfma_f32_16x16x32_bf16 v[4:7], v[164:167], v[206:209], v[4:7]
	s_barrier
	s_add_i32 s15, s15, 2
	s_add_u32 s20, s20, 0x100
	s_addc_u32 s21, s21, 0
	s_add_u32 s8, s8, 0x100
	s_addc_u32 s9, s9, 0
	s_cmp_gt_u32 s15, 29
	s_cbranch_scc0 .LBB0_594
	s_and_b64 vcc, exec, s[12:13]
	s_cbranch_vccz .LBB0_597
	s_barrier

.LBB0_700:
	ds_read_b128 v[120:123], v116
	ds_read_b128 v[132:135], v116 offset:1024
	ds_read_b128 v[144:147], v116 offset:2048
	ds_read_b128 v[148:151], v116 offset:3072
	ds_read_b128 v[152:155], v117
	ds_read_b128 v[156:159], v117 offset:1024
	ds_read_b128 v[166:169], v117 offset:2048
	ds_read_b128 v[170:173], v117 offset:3072
	s_add_u32 s27, s10, 0xfff7c080
	s_addc_u32 s47, s11, -1
	s_cmp_eq_u32 s26, 28
	s_cselect_b32 s49, s21, s47
	s_cselect_b32 s48, s20, s27
	s_cselect_b32 s51, s3, s25
	s_cselect_b32 s50, s4, s24
	s_mov_b32 m0, s5
	v_lshl_add_u64 v[208:209], s[10:11], 0, v[164:165]
	ds_read_b128 v[180:183], v178
	ds_read_b128 v[184:187], v178 offset:1024
	ds_read_b128 v[188:191], v178 offset:2048
	ds_read_b128 v[192:195], v178 offset:3072
	ds_read_b128 v[196:199], v178 offset:4096
	ds_read_b128 v[200:203], v178 offset:5120
	ds_read_b128 v[204:207], v178 offset:6144
	ds_read_b128 v[214:217], v178 offset:7168
	global_load_lds_dwordx4 v[208:209], off
	v_lshl_add_u64 v[208:209], v[208:209], 0, s[96:97]
	s_mov_b32 m0, s19
	s_nop 0
	global_load_lds_dwordx4 v[208:209], off
	s_waitcnt vmcnt(8)
	s_waitcnt lgkmcnt(0)
	s_barrier
	v_mfma_f32_16x16x32_bf16 v[140:143], v[120:123], v[180:183], v[140:143]
	v_mfma_f32_16x16x32_bf16 v[140:143], v[132:135], v[184:187], v[140:143]
	v_mfma_f32_16x16x32_bf16 v[136:139], v[144:147], v[180:183], v[136:139]
	v_mfma_f32_16x16x32_bf16 v[136:139], v[148:151], v[184:187], v[136:139]
	v_mfma_f32_16x16x32_bf16 v[128:131], v[152:155], v[180:183], v[128:131]
	v_mfma_f32_16x16x32_bf16 v[128:131], v[156:159], v[184:187], v[128:131]
	v_mfma_f32_16x16x32_bf16 v[124:127], v[166:169], v[180:183], v[124:127]
	v_mfma_f32_16x16x32_bf16 v[124:127], v[170:173], v[184:187], v[124:127]
	v_mfma_f32_16x16x32_bf16 v[112:115], v[120:123], v[188:191], v[112:115]
	v_mfma_f32_16x16x32_bf16 v[112:115], v[132:135], v[192:195], v[112:115]
	v_mfma_f32_16x16x32_bf16 v[108:111], v[144:147], v[188:191], v[108:111]
	v_mfma_f32_16x16x32_bf16 v[108:111], v[148:151], v[192:195], v[108:111]
	v_mfma_f32_16x16x32_bf16 v[104:107], v[152:155], v[188:191], v[104:107]
	v_mfma_f32_16x16x32_bf16 v[104:107], v[156:159], v[192:195], v[104:107]
	v_mfma_f32_16x16x32_bf16 v[100:103], v[166:169], v[188:191], v[100:103]
	v_mfma_f32_16x16x32_bf16 v[100:103], v[170:173], v[192:195], v[100:103]
	v_mfma_f32_16x16x32_bf16 v[96:99], v[120:123], v[196:199], v[96:99]
	v_mfma_f32_16x16x32_bf16 v[96:99], v[132:135], v[200:203], v[96:99]
	v_mfma_f32_16x16x32_bf16 v[92:95], v[144:147], v[196:199], v[92:95]
	v_mfma_f32_16x16x32_bf16 v[92:95], v[148:151], v[200:203], v[92:95]
	v_mfma_f32_16x16x32_bf16 v[88:91], v[152:155], v[196:199], v[88:91]
	v_mfma_f32_16x16x32_bf16 v[88:91], v[156:159], v[200:203], v[88:91]
	v_mfma_f32_16x16x32_bf16 v[84:87], v[166:169], v[196:199], v[84:87]
	v_mfma_f32_16x16x32_bf16 v[84:87], v[170:173], v[200:203], v[84:87]
	v_mfma_f32_16x16x32_bf16 v[80:83], v[120:123], v[204:207], v[80:83]
	v_mfma_f32_16x16x32_bf16 v[80:83], v[132:135], v[214:217], v[80:83]
	v_mfma_f32_16x16x32_bf16 v[76:79], v[144:147], v[204:207], v[76:79]
	v_mfma_f32_16x16x32_bf16 v[76:79], v[148:151], v[214:217], v[76:79]
	v_mfma_f32_16x16x32_bf16 v[72:75], v[152:155], v[204:207], v[72:75]
	v_mfma_f32_16x16x32_bf16 v[72:75], v[156:159], v[214:217], v[72:75]
	v_mfma_f32_16x16x32_bf16 v[68:71], v[166:169], v[204:207], v[68:71]
	v_mfma_f32_16x16x32_bf16 v[68:71], v[170:173], v[214:217], v[68:71]
	s_barrier
	s_mov_b32 m0, s33
	v_lshl_add_u64 v[208:209], s[50:51], 0, v[160:161]
	ds_read_b128 v[180:183], v178 offset:16384
	ds_read_b128 v[184:187], v178 offset:17408
	ds_read_b128 v[188:191], v178 offset:18432
	ds_read_b128 v[192:195], v178 offset:19456
	ds_read_b128 v[196:199], v178 offset:20480
	ds_read_b128 v[200:203], v178 offset:21504
	ds_read_b128 v[204:207], v178 offset:22528
	ds_read_b128 v[214:217], v178 offset:23552
	global_load_lds_dwordx4 v[208:209], off
	v_lshl_add_u64 v[218:219], v[208:209], 0, s[90:91]
	s_mov_b32 m0, s40
	s_nop 0
	global_load_lds_dwordx4 v[218:219], off
	v_lshl_add_u64 v[218:219], v[208:209], 0, s[52:53]
	s_mov_b32 m0, s41
	s_nop 0
	global_load_lds_dwordx4 v[218:219], off
	v_lshl_add_u64 v[218:219], v[208:209], 0, s[56:57]
	s_mov_b32 m0, s42
	s_nop 0
	global_load_lds_dwordx4 v[218:219], off
	v_lshl_add_u64 v[218:219], s[48:49], 0, v[162:163]
	s_mov_b32 m0, s29
	v_lshl_add_u64 v[220:221], v[218:219], 0, s[96:97]
	global_load_lds_dwordx4 v[218:219], off
	s_mov_b32 m0, s30
	s_nop 0
	global_load_lds_dwordx4 v[220:221], off
	s_waitcnt vmcnt(8)
	s_waitcnt lgkmcnt(0)
	s_barrier
	v_mfma_f32_16x16x32_bf16 v[56:59], v[120:123], v[180:183], v[56:59]
	v_mfma_f32_16x16x32_bf16 v[56:59], v[132:135], v[184:187], v[56:59]
	v_mfma_f32_16x16x32_bf16 v[52:55], v[144:147], v[180:183], v[52:55]
	v_mfma_f32_16x16x32_bf16 v[52:55], v[148:151], v[184:187], v[52:55]
	v_mfma_f32_16x16x32_bf16 v[64:67], v[152:155], v[180:183], v[64:67]
	v_mfma_f32_16x16x32_bf16 v[64:67], v[156:159], v[184:187], v[64:67]
	v_mfma_f32_16x16x32_bf16 v[60:63], v[166:169], v[180:183], v[60:63]
	v_mfma_f32_16x16x32_bf16 v[60:63], v[170:173], v[184:187], v[60:63]
	v_mfma_f32_16x16x32_bf16 v[48:51], v[120:123], v[188:191], v[48:51]
	v_mfma_f32_16x16x32_bf16 v[48:51], v[132:135], v[192:195], v[48:51]
	v_mfma_f32_16x16x32_bf16 v[44:47], v[144:147], v[188:191], v[44:47]
	v_mfma_f32_16x16x32_bf16 v[44:47], v[148:151], v[192:195], v[44:47]
	v_mfma_f32_16x16x32_bf16 v[40:43], v[152:155], v[188:191], v[40:43]
	v_mfma_f32_16x16x32_bf16 v[40:43], v[156:159], v[192:195], v[40:43]
	v_mfma_f32_16x16x32_bf16 v[36:39], v[166:169], v[188:191], v[36:39]
	v_mfma_f32_16x16x32_bf16 v[36:39], v[170:173], v[192:195], v[36:39]
	v_mfma_f32_16x16x32_bf16 v[32:35], v[120:123], v[196:199], v[32:35]
	v_mfma_f32_16x16x32_bf16 v[32:35], v[132:135], v[200:203], v[32:35]
	v_mfma_f32_16x16x32_bf16 v[28:31], v[144:147], v[196:199], v[28:31]
	v_mfma_f32_16x16x32_bf16 v[28:31], v[148:151], v[200:203], v[28:31]
	v_mfma_f32_16x16x32_bf16 v[24:27], v[152:155], v[196:199], v[24:27]
	v_mfma_f32_16x16x32_bf16 v[24:27], v[156:159], v[200:203], v[24:27]
	v_mfma_f32_16x16x32_bf16 v[20:23], v[166:169], v[196:199], v[20:23]
	v_mfma_f32_16x16x32_bf16 v[20:23], v[170:173], v[200:203], v[20:23]
	v_mfma_f32_16x16x32_bf16 v[16:19], v[120:123], v[204:207], v[16:19]
	v_mfma_f32_16x16x32_bf16 v[16:19], v[132:135], v[214:217], v[16:19]
	v_mfma_f32_16x16x32_bf16 v[12:15], v[144:147], v[204:207], v[12:15]
	v_mfma_f32_16x16x32_bf16 v[12:15], v[148:151], v[214:217], v[12:15]
	v_mfma_f32_16x16x32_bf16 v[8:11], v[152:155], v[204:207], v[8:11]
	v_mfma_f32_16x16x32_bf16 v[8:11], v[156:159], v[214:217], v[8:11]
	v_mfma_f32_16x16x32_bf16 v[4:7], v[166:169], v[204:207], v[4:7]
	v_mfma_f32_16x16x32_bf16 v[4:7], v[170:173], v[214:217], v[4:7]
	s_barrier
	ds_read_b128 v[120:123], v118
	ds_read_b128 v[132:135], v118 offset:1024
	ds_read_b128 v[144:147], v118 offset:2048
	ds_read_b128 v[148:151], v118 offset:3072
	ds_read_b128 v[152:155], v119
	ds_read_b128 v[156:159], v119 offset:1024
	ds_read_b128 v[166:169], v119 offset:2048
	ds_read_b128 v[170:173], v119 offset:3072
	s_mov_b32 m0, s31
	v_lshl_add_u64 v[220:221], v[218:219], 0, s[82:83]
	ds_read_b128 v[180:183], v178 offset:32768
	ds_read_b128 v[184:187], v178 offset:33792
	ds_read_b128 v[188:191], v178 offset:34816
	ds_read_b128 v[192:195], v178 offset:35840
	ds_read_b128 v[196:199], v178 offset:36864
	ds_read_b128 v[200:203], v178 offset:37888
	ds_read_b128 v[204:207], v178 offset:38912
	ds_read_b128 v[214:217], v178 offset:39936
	global_load_lds_dwordx4 v[220:221], off
	v_lshl_add_u64 v[220:221], v[218:219], 0, s[62:63]
	s_mov_b32 m0, s34
	s_nop 0
	global_load_lds_dwordx4 v[220:221], off
	s_waitcnt vmcnt(8)
	s_waitcnt lgkmcnt(0)
	s_barrier
	v_mfma_f32_16x16x32_bf16 v[140:143], v[120:123], v[180:183], v[140:143]
	v_mfma_f32_16x16x32_bf16 v[140:143], v[132:135], v[184:187], v[140:143]
	v_mfma_f32_16x16x32_bf16 v[136:139], v[144:147], v[180:183], v[136:139]
	v_mfma_f32_16x16x32_bf16 v[136:139], v[148:151], v[184:187], v[136:139]
	v_mfma_f32_16x16x32_bf16 v[128:131], v[152:155], v[180:183], v[128:131]
	v_mfma_f32_16x16x32_bf16 v[128:131], v[156:159], v[184:187], v[128:131]
	v_mfma_f32_16x16x32_bf16 v[124:127], v[166:169], v[180:183], v[124:127]
	v_mfma_f32_16x16x32_bf16 v[124:127], v[170:173], v[184:187], v[124:127]
	v_mfma_f32_16x16x32_bf16 v[112:115], v[120:123], v[188:191], v[112:115]
	v_mfma_f32_16x16x32_bf16 v[112:115], v[132:135], v[192:195], v[112:115]
	v_mfma_f32_16x16x32_bf16 v[108:111], v[144:147], v[188:191], v[108:111]
	v_mfma_f32_16x16x32_bf16 v[108:111], v[148:151], v[192:195], v[108:111]
	v_mfma_f32_16x16x32_bf16 v[104:107], v[152:155], v[188:191], v[104:107]
	v_mfma_f32_16x16x32_bf16 v[104:107], v[156:159], v[192:195], v[104:107]
	v_mfma_f32_16x16x32_bf16 v[100:103], v[166:169], v[188:191], v[100:103]
	v_mfma_f32_16x16x32_bf16 v[100:103], v[170:173], v[192:195], v[100:103]
	v_mfma_f32_16x16x32_bf16 v[96:99], v[120:123], v[196:199], v[96:99]
	v_mfma_f32_16x16x32_bf16 v[96:99], v[132:135], v[200:203], v[96:99]
	v_mfma_f32_16x16x32_bf16 v[92:95], v[144:147], v[196:199], v[92:95]
	v_mfma_f32_16x16x32_bf16 v[92:95], v[148:151], v[200:203], v[92:95]
	v_mfma_f32_16x16x32_bf16 v[88:91], v[152:155], v[196:199], v[88:91]
	v_mfma_f32_16x16x32_bf16 v[88:91], v[156:159], v[200:203], v[88:91]
	v_mfma_f32_16x16x32_bf16 v[84:87], v[166:169], v[196:199], v[84:87]
	v_mfma_f32_16x16x32_bf16 v[84:87], v[170:173], v[200:203], v[84:87]
	v_mfma_f32_16x16x32_bf16 v[80:83], v[120:123], v[204:207], v[80:83]
	v_mfma_f32_16x16x32_bf16 v[80:83], v[132:135], v[214:217], v[80:83]
	v_mfma_f32_16x16x32_bf16 v[76:79], v[144:147], v[204:207], v[76:79]
	v_mfma_f32_16x16x32_bf16 v[76:79], v[148:151], v[214:217], v[76:79]
	v_mfma_f32_16x16x32_bf16 v[72:75], v[152:155], v[204:207], v[72:75]
	v_mfma_f32_16x16x32_bf16 v[72:75], v[156:159], v[214:217], v[72:75]
	v_mfma_f32_16x16x32_bf16 v[68:71], v[166:169], v[204:207], v[68:71]
	v_mfma_f32_16x16x32_bf16 v[68:71], v[170:173], v[214:217], v[68:71]
	s_barrier
; #define PG8_MMA(ai, bj, At, Bt) do { __builtin_amdgcn_s_setprio(1); _Pragma("unroll") for (int m = 0; m < 4; ++m) _Pragma("unroll") for (int n = 0; n < 2; ++n) _Pragma("unroll") for (int k = 0; k < 2; ++k) \
;         acc[ai][bj][m][n] = __builtin_amdgcn_mfma_f32_16x16x32_bf16(Bt[n][k], At[m][k], acc[ai][bj][m][n], 0, 0, 0); __builtin_amdgcn_s_setprio(0); } while (0)
; #define PG8_WAIT_V(n) asm volatile("s_waitcnt vmcnt(" #n ")" ::: "memory")
; #define PG8_TRIP_HEAD(T) const int t = (T); const bool last = (t == nt - 2); \
;             const char* a1 = cA + (size_t)(t + 1) * kstep; \
;             const char* a2 = last ? nA : cA + (size_t)(t + 2) * kstep; const char* b2 = last ? nB : cB + (size_t)(t + 2) * kstep; \
;             const char* a3 = a2 + kstep; const char* b3 = b2 + kstep; \
;             if (last && has_next) S.a_ready(nxt);
; template <class Epi, class Sched, bool ALIGN_EPI = false, bool SP2 = false>
; __device__ __forceinline__ void gemm_phase(PG8_LAS unsigned char* lds, const Gemm g, const Sched& S, const Epi& E) {
;     ...
;         if constexpr (SP2) {
;             { PG8_TRIP_HEAD(0) PG8_TRIP_SP2(asm volatile("s_waitcnt vmcnt(%0)" :: "n"(8 + Epi::NST) : "memory"), PG8_MMAZ) }
;             for (int tt = 2; tt < nt; tt += 2) { PG8_TRIP_HEAD(tt) PG8_TRIP_SP2(PG8_WAIT_V(8), PG8_MMA) }
	s_mov_b32 m0, s43
	v_lshl_add_u64 v[220:221], v[208:209], 0, s[78:79]
	ds_read_b128 v[180:183], v178 offset:49152
	ds_read_b128 v[184:187], v178 offset:50176
	ds_read_b128 v[188:191], v178 offset:51200
	ds_read_b128 v[192:195], v178 offset:52224
	ds_read_b128 v[196:199], v178 offset:53248
	ds_read_b128 v[200:203], v178 offset:54272
	ds_read_b128 v[204:207], v178 offset:55296
	ds_read_b128 v[214:217], v178 offset:56320
	global_load_lds_dwordx4 v[220:221], off
	v_lshl_add_u64 v[220:221], v[208:209], 0, s[84:85]
	s_mov_b32 m0, s44
	s_nop 0
	global_load_lds_dwordx4 v[220:221], off
	v_lshl_add_u64 v[220:221], v[208:209], 0, s[54:55]
	s_mov_b32 m0, s45
	v_lshl_add_u64 v[208:209], v[208:209], 0, s[60:61]
	global_load_lds_dwordx4 v[220:221], off
	s_mov_b32 m0, s46
	s_nop 0
	global_load_lds_dwordx4 v[208:209], off
	v_lshl_add_u64 v[208:209], v[218:219], 0, s[78:79]
	s_mov_b32 m0, s36
	s_nop 0
	global_load_lds_dwordx4 v[208:209], off
	v_lshl_add_u64 v[208:209], v[218:219], 0, s[92:93]
	s_mov_b32 m0, s37
	s_nop 0
	global_load_lds_dwordx4 v[208:209], off
	s_waitcnt vmcnt(8)
	s_waitcnt lgkmcnt(0)
	s_barrier
	v_mfma_f32_16x16x32_bf16 v[56:59], v[120:123], v[180:183], v[56:59]
	v_mfma_f32_16x16x32_bf16 v[56:59], v[132:135], v[184:187], v[56:59]
	v_mfma_f32_16x16x32_bf16 v[52:55], v[144:147], v[180:183], v[52:55]
	v_mfma_f32_16x16x32_bf16 v[52:55], v[148:151], v[184:187], v[52:55]
	v_mfma_f32_16x16x32_bf16 v[64:67], v[152:155], v[180:183], v[64:67]
	v_mfma_f32_16x16x32_bf16 v[64:67], v[156:159], v[184:187], v[64:67]
	v_mfma_f32_16x16x32_bf16 v[60:63], v[166:169], v[180:183], v[60:63]
	v_mfma_f32_16x16x32_bf16 v[60:63], v[170:173], v[184:187], v[60:63]
	v_mfma_f32_16x16x32_bf16 v[48:51], v[120:123], v[188:191], v[48:51]
	v_mfma_f32_16x16x32_bf16 v[48:51], v[132:135], v[192:195], v[48:51]
	v_mfma_f32_16x16x32_bf16 v[44:47], v[144:147], v[188:191], v[44:47]
	v_mfma_f32_16x16x32_bf16 v[44:47], v[148:151], v[192:195], v[44:47]
	v_mfma_f32_16x16x32_bf16 v[40:43], v[152:155], v[188:191], v[40:43]
	v_mfma_f32_16x16x32_bf16 v[40:43], v[156:159], v[192:195], v[40:43]
	v_mfma_f32_16x16x32_bf16 v[36:39], v[166:169], v[188:191], v[36:39]
	v_mfma_f32_16x16x32_bf16 v[36:39], v[170:173], v[192:195], v[36:39]
	v_mfma_f32_16x16x32_bf16 v[32:35], v[120:123], v[196:199], v[32:35]
	v_mfma_f32_16x16x32_bf16 v[32:35], v[132:135], v[200:203], v[32:35]
	v_mfma_f32_16x16x32_bf16 v[28:31], v[144:147], v[196:199], v[28:31]
	v_mfma_f32_16x16x32_bf16 v[28:31], v[148:151], v[200:203], v[28:31]
	v_mfma_f32_16x16x32_bf16 v[24:27], v[152:155], v[196:199], v[24:27]
	v_mfma_f32_16x16x32_bf16 v[24:27], v[156:159], v[200:203], v[24:27]
	v_mfma_f32_16x16x32_bf16 v[20:23], v[166:169], v[196:199], v[20:23]
	v_mfma_f32_16x16x32_bf16 v[20:23], v[170:173], v[200:203], v[20:23]
	v_mfma_f32_16x16x32_bf16 v[16:19], v[120:123], v[204:207], v[16:19]
	v_mfma_f32_16x16x32_bf16 v[16:19], v[132:135], v[214:217], v[16:19]
	v_mfma_f32_16x16x32_bf16 v[12:15], v[144:147], v[204:207], v[12:15]
	v_mfma_f32_16x16x32_bf16 v[12:15], v[148:151], v[214:217], v[12:15]
	v_mfma_f32_16x16x32_bf16 v[8:11], v[152:155], v[204:207], v[8:11]
	v_mfma_f32_16x16x32_bf16 v[8:11], v[156:159], v[214:217], v[8:11]
	v_mfma_f32_16x16x32_bf16 v[4:7], v[166:169], v[204:207], v[4:7]
	v_mfma_f32_16x16x32_bf16 v[4:7], v[170:173], v[214:217], v[4:7]
	s_barrier
	s_add_i32 s26, s26, 2
	s_add_u32 s10, s10, 0x100
	s_addc_u32 s11, s11, 0
	s_add_u32 s24, s24, 0x100
	s_addc_u32 s25, s25, 0
	s_cmp_gt_u32 s26, 29
	s_cbranch_scc0 .LBB0_700
	s_and_b64 vcc, exec, s[16:17]
	s_cbranch_vccz .LBB0_703
	s_barrier
